# stack: memkv move, mlstm_c q prefetch, gates waits, non-temporal hints on prologue and combine streams, DMA split in fp8 GEMM loops
# speedup vs baseline: 1.0101x; 1.0101x over previous
.LBB0_13:
	s_mov_b64 s[6:7], s[0:1]
	s_load_dwordx2 s[26:27], s[6:7], 0x0
	s_mov_b64 s[6:7], s[0:1]
	s_add_i32 s8, s31, 0x4000
	s_ashr_i32 s9, s8, 31
	s_waitcnt lgkmcnt(0)
	v_lshl_add_u64 v[2:3], s[26:27], 0, v[52:53]
	global_load_dwordx4 v[34:37], v[2:3], off offset:-4096 nt
	global_load_dwordx4 v[30:33], v[2:3], off offset:-3072 nt
	global_load_dwordx4 v[18:21], v[2:3], off offset:-2048 nt
	global_load_dwordx4 v[10:13], v[2:3], off offset:-1024 nt
	s_load_dwordx2 s[26:27], s[6:7], 0x0
	s_lshl_b64 s[6:7], s[8:9], 11
	s_lshl_b64 s[34:35], s[8:9], 13
	v_add_co_u32_e32 v4, vcc, s3, v2
	s_waitcnt lgkmcnt(0)
	s_add_u32 s26, s26, s34
	s_addc_u32 s27, s27, s35
	v_addc_co_u32_e32 v5, vcc, -1, v3, vcc
	v_lshl_add_u64 v[6:7], s[26:27], 0, v[42:43]
	global_load_dwordx4 v[66:69], v[4:5], off offset:-3072 nt
	global_load_dwordx4 v[70:73], v[4:5], off offset:-2048 nt
	v_add_co_u32_e32 v90, vcc, s13, v6
	global_load_dwordx4 v[74:77], v[4:5], off offset:-1024 nt
	s_nop 0
	v_addc_co_u32_e32 v91, vcc, 0, v7, vcc
	global_load_dwordx4 v[2:5], v[2:3], off nt
	s_nop 0
	global_load_dwordx4 v[78:81], v42, s[26:27] nt
	global_load_dwordx4 v[82:85], v42, s[26:27] offset:1024 nt
	global_load_dwordx4 v[86:89], v42, s[26:27] offset:2048 nt
	global_load_dwordx4 v[38:41], v42, s[26:27] offset:3072 nt
	global_load_dwordx4 v[26:29], v[90:91], off nt
	global_load_dwordx4 v[22:25], v[90:91], off offset:1024 nt
	global_load_dwordx4 v[14:17], v[90:91], off offset:2048 nt
	global_load_dwordx4 v[6:9], v[90:91], off offset:3072 nt
	v_lshl_add_u64 v[90:91], s[82:83], 0, v[48:49]
	v_add_co_u32_e32 v90, vcc, s15, v90
	s_lshl_b64 s[8:9], s[8:9], 12
	s_nop 0
	v_addc_co_u32_e32 v91, vcc, 0, v91, vcc
	v_lshl_add_u64 v[92:93], v[44:45], 0, s[8:9]
	s_waitcnt vmcnt(15)
	v_cvt_pk_bf16_f32 v94, v34, v35
	v_cvt_pk_bf16_f32 v95, v36, v37
	s_waitcnt vmcnt(14)
	v_cvt_pk_bf16_f32 v96, v30, v31
	v_cvt_pk_bf16_f32 v97, v32, v33
	s_waitcnt vmcnt(13)
	v_cvt_pk_bf16_f32 v98, v18, v19
	v_cvt_pk_bf16_f32 v99, v20, v21
	s_waitcnt vmcnt(12)
	v_cvt_pk_bf16_f32 v100, v10, v11
	v_cvt_pk_bf16_f32 v101, v12, v13
	s_waitcnt vmcnt(11)
	v_cvt_pk_bf16_f32 v102, v66, v67
	v_cvt_pk_bf16_f32 v103, v68, v69
	s_waitcnt vmcnt(10)
	v_cvt_pk_bf16_f32 v105, v72, v73
	global_store_dwordx2 v[90:91], v[102:103], off nt
	v_cvt_pk_bf16_f32 v104, v70, v71
	s_waitcnt vmcnt(8)
	v_cvt_pk_bf16_f32 v102, v78, v79
	v_cvt_pk_bf16_f32 v103, v80, v81
	v_cvt_pk_bf16_f32 v106, v74, v75
	v_cvt_pk_bf16_f32 v107, v76, v77
	v_mul_f32_e32 v116, v67, v67
	s_waitcnt vmcnt(7)
	v_cvt_pk_bf16_f32 v110, v82, v83
	v_cvt_pk_bf16_f32 v111, v84, v85
	s_waitcnt vmcnt(6)
	v_cvt_pk_bf16_f32 v112, v86, v87
	v_cvt_pk_bf16_f32 v113, v88, v89
	s_waitcnt vmcnt(5)
	v_cvt_pk_bf16_f32 v114, v38, v39
	v_cvt_pk_bf16_f32 v115, v40, v41
	global_store_dwordx2 v[92:93], v[102:103], off nt
	global_store_dwordx2 v[90:91], v[104:105], off offset:512 nt
	global_store_dwordx2 v[92:93], v[110:111], off offset:512 nt
	global_store_dwordx2 v[90:91], v[106:107], off offset:1024 nt
	global_store_dwordx2 v[92:93], v[112:113], off offset:1024 nt
	global_store_dwordx2 v[90:91], v[94:95], off offset:1536 nt
	global_store_dwordx2 v[92:93], v[114:115], off offset:1536 nt
	global_store_dwordx2 v[90:91], v[96:97], off offset:2048 nt
	s_waitcnt vmcnt(12)
	v_cvt_pk_bf16_f32 v94, v26, v27
	v_cvt_pk_bf16_f32 v95, v28, v29
	s_waitcnt vmcnt(9)
	v_cvt_pk_bf16_f32 v105, v8, v9
	v_cvt_pk_bf16_f32 v108, v2, v3
	v_cvt_pk_bf16_f32 v109, v4, v5
	v_cvt_pk_bf16_f32 v96, v22, v23
	v_cvt_pk_bf16_f32 v97, v24, v25
	v_cvt_pk_bf16_f32 v102, v14, v15
	v_cvt_pk_bf16_f32 v103, v16, v17
	v_cvt_pk_bf16_f32 v104, v6, v7
	global_store_dwordx2 v[92:93], v[94:95], off offset:2048 nt
	global_store_dwordx2 v[90:91], v[98:99], off offset:2560 nt
	global_store_dwordx2 v[92:93], v[96:97], off offset:2560 nt
	global_store_dwordx2 v[90:91], v[100:101], off offset:3072 nt
	global_store_dwordx2 v[92:93], v[102:103], off offset:3072 nt
	global_store_dwordx2 v[90:91], v[108:109], off offset:3584 nt
	global_store_dwordx2 v[92:93], v[104:105], off offset:3584 nt
	v_fmac_f32_e32 v116, v66, v66
	v_mul_f32_e32 v90, v69, v69
	v_mul_f32_e32 v66, 4.0, v66
	v_mul_f32_e32 v67, 4.0, v67
	v_mul_f32_e32 v91, v79, v79
	v_mul_f32_e32 v105, v31, v31
	v_fmac_f32_e32 v90, v68, v68
	v_mul_f32_e32 v68, 4.0, v68
	v_mul_f32_e32 v69, 4.0, v69
	v_fmac_f32_e32 v91, v78, v78
	v_mul_f32_e32 v78, 4.0, v78
	v_mul_f32_e32 v79, 4.0, v79
	v_mul_f32_e32 v93, v71, v71
	v_fmac_f32_e32 v105, v30, v30
	v_mul_f32_e32 v107, 4.0, v30
	v_mul_f32_e32 v108, 4.0, v31
	v_med3_f32 v30, v66, s28, v61
	v_med3_f32 v31, v67, s28, v61
	v_mov_b32_e32 v66, 0
	v_fmac_f32_e32 v93, v70, v70
	v_mul_f32_e32 v70, 4.0, v70
	v_mul_f32_e32 v71, 4.0, v71
	v_cvt_pk_fp8_f32 v66, v30, v31
	v_med3_f32 v30, v68, s28, v61
	v_med3_f32 v31, v69, s28, v61
	v_med3_f32 v67, v78, s28, v61
	v_med3_f32 v68, v79, s28, v61
	v_mov_b32_e32 v69, 0
	v_cvt_pk_fp8_f32 v69, v67, v68
	v_med3_f32 v67, v70, s28, v61
	v_med3_f32 v68, v71, s28, v61
	v_mov_b32_e32 v70, 0
	v_mul_f32_e32 v92, v81, v81
	v_cvt_pk_fp8_f32 v70, v67, v68
	v_fmac_f32_e32 v92, v80, v80
	v_mul_f32_e32 v80, 4.0, v80
	v_mul_f32_e32 v81, 4.0, v81
	v_mul_f32_e32 v94, v73, v73
	v_fmac_f32_e32 v94, v72, v72
	v_mul_f32_e32 v72, 4.0, v72
	v_mul_f32_e32 v73, 4.0, v73
	v_mul_f32_e32 v95, v83, v83
	v_med3_f32 v67, v80, s28, v61
	v_med3_f32 v68, v81, s28, v61
	v_fmac_f32_e32 v95, v82, v82
	v_mul_f32_e32 v82, 4.0, v82
	v_mul_f32_e32 v83, 4.0, v83
	v_mul_f32_e32 v97, v75, v75
	v_cvt_pk_fp8_f32 v69, v67, v68 op_sel:[0,0,1]
	v_med3_f32 v67, v72, s28, v61
	v_med3_f32 v68, v73, s28, v61
	v_fmac_f32_e32 v97, v74, v74
	v_mul_f32_e32 v74, 4.0, v74
	v_mul_f32_e32 v75, 4.0, v75
	v_cvt_pk_fp8_f32 v70, v67, v68 op_sel:[0,0,1]
	v_med3_f32 v67, v82, s28, v61
	v_med3_f32 v68, v83, s28, v61
	v_mov_b32_e32 v71, 0
	v_cvt_pk_fp8_f32 v71, v67, v68
	v_med3_f32 v67, v74, s28, v61
	v_med3_f32 v68, v75, s28, v61
	v_mov_b32_e32 v72, 0
	v_mul_f32_e32 v96, v85, v85
	v_cvt_pk_fp8_f32 v72, v67, v68
	v_fmac_f32_e32 v96, v84, v84
	v_mul_f32_e32 v84, 4.0, v84
	v_mul_f32_e32 v85, 4.0, v85
	v_mul_f32_e32 v98, v77, v77
	v_fmac_f32_e32 v98, v76, v76
	v_mul_f32_e32 v76, 4.0, v76
	v_mul_f32_e32 v77, 4.0, v77
	v_mul_f32_e32 v99, v87, v87
	v_med3_f32 v67, v84, s28, v61
	v_med3_f32 v68, v85, s28, v61
	v_fmac_f32_e32 v99, v86, v86
	v_mul_f32_e32 v86, 4.0, v86
	v_mul_f32_e32 v87, 4.0, v87
	v_mul_f32_e32 v101, v35, v35
	v_cvt_pk_fp8_f32 v71, v67, v68 op_sel:[0,0,1]
	v_med3_f32 v67, v76, s28, v61
	v_med3_f32 v68, v77, s28, v61
	v_fmac_f32_e32 v101, v34, v34
	v_mul_f32_e32 v34, 4.0, v34
	v_mul_f32_e32 v35, 4.0, v35
	v_cvt_pk_fp8_f32 v72, v67, v68 op_sel:[0,0,1]
	v_med3_f32 v67, v86, s28, v61
	v_med3_f32 v68, v87, s28, v61
	v_mov_b32_e32 v73, 0
	v_cvt_pk_fp8_f32 v73, v67, v68
	v_med3_f32 v34, v34, s28, v61
	v_med3_f32 v35, v35, s28, v61
	v_mov_b32_e32 v67, 0
	v_mul_f32_e32 v100, v89, v89
	v_cvt_pk_fp8_f32 v67, v34, v35
	v_fmac_f32_e32 v100, v88, v88
	v_mul_f32_e32 v88, 4.0, v88
	v_mul_f32_e32 v89, 4.0, v89
	v_mul_f32_e32 v102, v37, v37
	v_fmac_f32_e32 v102, v36, v36
	v_mul_f32_e32 v36, 4.0, v36
	v_mul_f32_e32 v37, 4.0, v37
	v_mul_f32_e32 v103, v39, v39
	v_med3_f32 v34, v88, s28, v61
	v_med3_f32 v35, v89, s28, v61
	v_fmac_f32_e32 v103, v38, v38
	v_mul_f32_e32 v38, 4.0, v38
	v_mul_f32_e32 v39, 4.0, v39
	v_cvt_pk_fp8_f32 v73, v34, v35 op_sel:[0,0,1]
	v_med3_f32 v34, v36, s28, v61
	v_med3_f32 v35, v37, s28, v61
	v_cvt_pk_fp8_f32 v67, v34, v35 op_sel:[0,0,1]
	v_med3_f32 v34, v38, s28, v61
	v_med3_f32 v35, v39, s28, v61
	v_mov_b32_e32 v36, 0
	v_cvt_pk_fp8_f32 v36, v34, v35
	v_mul_f32_e32 v104, v41, v41
	v_fmac_f32_e32 v104, v40, v40
	v_mul_f32_e32 v40, 4.0, v40
	v_mul_f32_e32 v41, 4.0, v41
	v_med3_f32 v34, v107, s28, v61
	v_med3_f32 v35, v108, s28, v61
	v_mov_b32_e32 v37, 0
	v_cvt_pk_fp8_f32 v37, v34, v35
	v_med3_f32 v34, v40, s28, v61
	v_med3_f32 v35, v41, s28, v61
	v_cvt_pk_fp8_f32 v36, v34, v35 op_sel:[0,0,1]
	v_add_f32_e32 v34, v116, v90
	v_add_f32_e32 v38, v93, v94
	v_add_f32_e32 v35, v91, v92
	v_add_f32_e32 v34, v34, v38
	v_add_f32_e32 v38, v95, v96
	v_add_f32_e32 v35, v35, v38
	v_add_f32_e32 v38, v97, v98
	v_add_f32_e32 v34, v34, v38
	v_add_f32_e32 v38, v99, v100
	v_mul_f32_e32 v106, v33, v33
	v_add_f32_e32 v35, v35, v38
	v_add_f32_e32 v38, v101, v102
	v_fmac_f32_e32 v106, v32, v32
	v_add_f32_e32 v34, v34, v38
	v_add_f32_e32 v38, v103, v104
	v_add_f32_e32 v35, v35, v38
	v_add_f32_e32 v38, v105, v106
	v_add_f32_e32 v34, v34, v38
	v_mul_f32_e32 v38, v27, v27
	v_mul_f32_e32 v39, v29, v29
	v_fmac_f32_e32 v38, v26, v26
	v_fmac_f32_e32 v39, v28, v28
	v_add_f32_e32 v38, v38, v39
	v_add_f32_e32 v35, v35, v38
	v_mul_f32_e32 v38, v19, v19
	v_mul_f32_e32 v39, v21, v21
	v_fmac_f32_e32 v38, v18, v18
	v_fmac_f32_e32 v39, v20, v20
	v_add_f32_e32 v38, v38, v39
	v_add_f32_e32 v34, v34, v38
	v_mul_f32_e32 v38, v23, v23
	v_mul_f32_e32 v39, v25, v25
	v_fmac_f32_e32 v38, v22, v22
	v_fmac_f32_e32 v39, v24, v24
	v_add_f32_e32 v38, v38, v39
	v_cvt_pk_fp8_f32 v66, v30, v31 op_sel:[0,0,1]
	v_lshl_add_u64 v[30:31], s[82:83], 0, v[50:51]
	v_add_f32_e32 v35, v35, v38
	v_mul_f32_e32 v38, v11, v11
	v_mul_f32_e32 v39, v13, v13
	v_add_co_u32_e32 v30, vcc, s29, v30
	v_fmac_f32_e32 v38, v10, v10
	v_fmac_f32_e32 v39, v12, v12
	v_mul_f32_e32 v40, v3, v3
	v_mul_f32_e32 v41, v5, v5
	v_addc_co_u32_e32 v31, vcc, 0, v31, vcc
	v_add_f32_e32 v38, v38, v39
	v_fmac_f32_e32 v40, v2, v2
	v_fmac_f32_e32 v41, v4, v4
	v_add_f32_e32 v34, v34, v38
	v_add_f32_e32 v40, v40, v41
	v_cmp_lt_i32_e32 vcc, v55, v54
	v_add_f32_e32 v34, v34, v40
	v_mul_f32_e32 v38, v15, v15
	v_cndmask_b32_e32 v40, v1, v55, vcc
	v_lshlrev_b32_e32 v40, 2, v40
	ds_bpermute_b32 v41, v40, v34
	v_mul_f32_e32 v39, v17, v17
	v_fmac_f32_e32 v38, v14, v14
	v_fmac_f32_e32 v39, v16, v16
	v_cmp_lt_i32_e32 vcc, v56, v54
	v_add_f32_e32 v38, v38, v39
	s_waitcnt lgkmcnt(0)
	v_add_f32_e32 v34, v34, v41
	v_cndmask_b32_e32 v39, v1, v56, vcc
	v_lshlrev_b32_e32 v39, 2, v39
	ds_bpermute_b32 v41, v39, v34
	v_add_f32_e32 v35, v35, v38
	v_mul_f32_e32 v38, v7, v7
	v_mul_f32_e32 v68, v9, v9
	v_fmac_f32_e32 v38, v6, v6
	v_fmac_f32_e32 v68, v8, v8
	v_add_f32_e32 v38, v38, v68
	v_cmp_lt_i32_e32 vcc, v57, v54
	v_add_f32_e32 v35, v35, v38
	s_waitcnt lgkmcnt(0)
	v_add_f32_e32 v34, v34, v41
	v_cndmask_b32_e32 v38, v1, v57, vcc
	v_lshlrev_b32_e32 v38, 2, v38
	ds_bpermute_b32 v40, v40, v35
	ds_bpermute_b32 v41, v38, v34
	v_mul_f32_e32 v32, 4.0, v32
	v_mul_f32_e32 v33, 4.0, v33
	v_med3_f32 v32, v32, s28, v61
	v_med3_f32 v33, v33, s28, v61
	v_cmp_lt_i32_e32 vcc, v58, v54
	v_cvt_pk_fp8_f32 v37, v32, v33 op_sel:[0,0,1]
	s_waitcnt lgkmcnt(1)
	v_add_f32_e32 v33, v35, v40
	v_cndmask_b32_e32 v35, v1, v58, vcc
	s_waitcnt lgkmcnt(0)
	v_add_f32_e32 v32, v34, v41
	v_lshlrev_b32_e32 v35, 2, v35
	ds_bpermute_b32 v34, v39, v33
	ds_bpermute_b32 v39, v35, v32
	v_mul_f32_e32 v26, 4.0, v26
	v_mul_f32_e32 v27, 4.0, v27
	v_med3_f32 v26, v26, s28, v61
	v_med3_f32 v27, v27, s28, v61
	s_waitcnt lgkmcnt(0)
	v_add_f32_e32 v32, v32, v39
	v_mov_b32_e32 v39, 0
	v_cvt_pk_fp8_f32 v39, v26, v27
	v_mul_f32_e32 v28, 4.0, v28
	v_mul_f32_e32 v29, 4.0, v29
	v_med3_f32 v28, v28, s28, v61
	v_med3_f32 v29, v29, s28, v61
	v_mul_f32_e32 v18, 4.0, v18
	v_mul_f32_e32 v19, 4.0, v19
	v_cvt_pk_fp8_f32 v39, v28, v29 op_sel:[0,0,1]
	v_med3_f32 v18, v18, s28, v61
	v_med3_f32 v19, v19, s28, v61
	v_mov_b32_e32 v28, 0
	v_cvt_pk_fp8_f32 v28, v18, v19
	v_mul_f32_e32 v20, 4.0, v20
	v_mul_f32_e32 v18, 4.0, v21
	v_med3_f32 v19, v20, s28, v61
	v_med3_f32 v18, v18, s28, v61
	v_cvt_pk_fp8_f32 v28, v19, v18 op_sel:[0,0,1]
	v_mul_f32_e32 v18, 4.0, v22
	v_mul_f32_e32 v19, 4.0, v23
	v_med3_f32 v18, v18, s28, v61
	v_med3_f32 v19, v19, s28, v61
	v_mov_b32_e32 v21, 0
	v_cvt_pk_fp8_f32 v21, v18, v19
	v_mul_f32_e32 v20, 4.0, v24
	v_mul_f32_e32 v18, 4.0, v25
	v_add_f32_e32 v33, v33, v34
	v_med3_f32 v19, v20, s28, v61
	v_med3_f32 v18, v18, s28, v61
	v_mul_f32_e32 v10, 4.0, v10
	v_mul_f32_e32 v11, 4.0, v11
	ds_bpermute_b32 v34, v38, v33
	v_cvt_pk_fp8_f32 v21, v19, v18 op_sel:[0,0,1]
	v_med3_f32 v10, v10, s28, v61
	v_med3_f32 v11, v11, s28, v61
	v_mov_b32_e32 v18, 0
	v_cvt_pk_fp8_f32 v18, v10, v11
	v_mul_f32_e32 v12, 4.0, v12
	v_mul_f32_e32 v10, 4.0, v13
	v_med3_f32 v11, v12, s28, v61
	v_med3_f32 v10, v10, s28, v61
	s_waitcnt lgkmcnt(0)
	v_add_f32_e32 v33, v33, v34
	v_cvt_pk_fp8_f32 v18, v11, v10 op_sel:[0,0,1]
	v_mul_f32_e32 v10, 4.0, v14
	v_mul_f32_e32 v11, 4.0, v15
	ds_bpermute_b32 v34, v35, v33
	v_med3_f32 v10, v10, s28, v61
	v_med3_f32 v11, v11, s28, v61
	v_mov_b32_e32 v13, 0
	v_cvt_pk_fp8_f32 v13, v10, v11
	v_cmp_lt_i32_e32 vcc, v59, v54
	v_mul_f32_e32 v12, 4.0, v16
	v_mul_f32_e32 v10, 4.0, v17
	v_cndmask_b32_e32 v35, v1, v59, vcc
	v_med3_f32 v11, v12, s28, v61
	v_med3_f32 v10, v10, s28, v61
	v_mul_f32_e32 v2, 4.0, v2
	v_mul_f32_e32 v3, 4.0, v3
	v_lshlrev_b32_e32 v35, 2, v35
	s_waitcnt lgkmcnt(0)
	v_add_f32_e32 v33, v33, v34
	v_cvt_pk_fp8_f32 v13, v11, v10 op_sel:[0,0,1]
	v_med3_f32 v2, v2, s28, v61
	v_med3_f32 v3, v3, s28, v61
	v_mov_b32_e32 v10, 0
	ds_bpermute_b32 v38, v35, v32
	ds_bpermute_b32 v34, v35, v33
	v_cvt_pk_fp8_f32 v10, v2, v3
	v_mul_f32_e32 v4, 4.0, v4
	v_mul_f32_e32 v2, 4.0, v5
	v_cmp_lt_i32_e32 vcc, v60, v54
	v_med3_f32 v3, v4, s28, v61
	v_med3_f32 v2, v2, s28, v61
	v_cndmask_b32_e32 v27, v1, v60, vcc
	v_cvt_pk_fp8_f32 v10, v3, v2 op_sel:[0,0,1]
	v_mul_f32_e32 v2, 4.0, v6
	v_mul_f32_e32 v3, 4.0, v7
	s_waitcnt lgkmcnt(1)
	v_add_f32_e32 v32, v32, v38
	s_waitcnt lgkmcnt(0)
	v_add_f32_e32 v26, v33, v34
	v_lshlrev_b32_e32 v27, 2, v27
	v_med3_f32 v2, v2, s28, v61
	v_med3_f32 v3, v3, s28, v61
	v_mov_b32_e32 v5, 0
	ds_bpermute_b32 v33, v27, v32
	ds_bpermute_b32 v27, v27, v26
	v_cvt_pk_fp8_f32 v5, v2, v3
	v_mul_f32_e32 v4, 4.0, v8
	v_mul_f32_e32 v2, 4.0, v9
	v_med3_f32 v3, v4, s28, v61
	v_med3_f32 v2, v2, s28, v61
	v_lshl_add_u64 v[34:35], v[46:47], 0, s[6:7]
	v_cvt_pk_fp8_f32 v5, v3, v2 op_sel:[0,0,1]
	global_store_dword v[30:31], v66, off
	global_store_dword v[34:35], v69, off
	global_store_dword v[30:31], v70, off offset:256
	global_store_dword v[34:35], v71, off offset:256
	global_store_dword v[30:31], v72, off offset:512
	global_store_dword v[34:35], v73, off offset:512
	global_store_dword v[30:31], v67, off offset:768
	global_store_dword v[34:35], v36, off offset:768
	global_store_dword v[30:31], v37, off offset:1024
	global_store_dword v[34:35], v39, off offset:1024
	global_store_dword v[30:31], v28, off offset:1280
	global_store_dword v[34:35], v21, off offset:1280
	global_store_dword v[30:31], v18, off offset:1536
	global_store_dword v[34:35], v13, off offset:1536
	global_store_dword v[30:31], v10, off offset:1792
	global_store_dword v[34:35], v5, off offset:1792
	s_and_saveexec_b64 s[26:27], s[4:5]
	s_cbranch_execz .LBB0_12
	s_waitcnt lgkmcnt(1)
	v_add_f32_e32 v2, v32, v33
	v_fmamk_f32 v2, v2, 0x3a000000, v62
	v_mul_f32_e32 v3, 0x4f800000, v2
	v_cmp_gt_f32_e32 vcc, s30, v2
	s_add_u32 s34, s82, s16
	s_addc_u32 s35, s83, s17
	v_cndmask_b32_e32 v2, v2, v3, vcc
	v_sqrt_f32_e32 v3, v2
	s_nop 0
	v_add_u32_e32 v4, -1, v3
	v_fma_f32 v6, -v4, v3, v2
	v_add_u32_e32 v5, 1, v3
	v_cmp_ge_f32_e64 s[6:7], 0, v6
	s_nop 1
	v_cndmask_b32_e64 v4, v3, v4, s[6:7]
	v_fma_f32 v3, -v5, v3, v2
	v_cmp_lt_f32_e64 s[6:7], 0, v3
	s_nop 1
	v_cndmask_b32_e64 v3, v4, v5, s[6:7]
	v_mul_f32_e32 v4, 0x37800000, v3
	v_cndmask_b32_e32 v3, v3, v4, vcc
	v_cmp_class_f32_e32 vcc, v2, v63
	s_waitcnt lgkmcnt(0)
	v_add_f32_e32 v5, v26, v27
	v_fmamk_f32 v5, v5, 0x3a000000, v62
	v_cndmask_b32_e32 v2, v3, v2, vcc
	v_div_scale_f32 v3, s[6:7], v2, v2, 1.0
	v_rcp_f32_e32 v4, v3
	v_mul_f32_e32 v8, 0x4f800000, v5
	v_cmp_gt_f32_e64 s[6:7], s30, v5
	v_fma_f32 v6, -v3, v4, 1.0
	s_nop 0
	v_cndmask_b32_e64 v5, v5, v8, s[6:7]
	v_fmac_f32_e32 v4, v6, v4
	v_div_scale_f32 v6, vcc, 1.0, v2, 1.0
	v_sqrt_f32_e32 v8, v5
	v_mul_f32_e32 v7, v6, v4
	v_fma_f32 v9, -v3, v7, v6
	v_fmac_f32_e32 v7, v9, v4
	v_fma_f32 v3, -v3, v7, v6
	v_add_u32_e32 v6, -1, v8
	v_fma_f32 v9, -v6, v8, v5
	v_cmp_ge_f32_e64 s[8:9], 0, v9
	v_add_u32_e32 v9, 1, v8
	v_div_fmas_f32 v3, v3, v4, v7
	v_cndmask_b32_e64 v6, v8, v6, s[8:9]
	v_fma_f32 v8, -v9, v8, v5
	v_cmp_lt_f32_e64 s[8:9], 0, v8
	v_div_fixup_f32 v2, v3, v2, 1.0
	global_store_dword v64, v2, s[34:35]
	v_cndmask_b32_e64 v6, v6, v9, s[8:9]
	v_mul_f32_e32 v8, 0x37800000, v6
	v_cndmask_b32_e64 v6, v6, v8, s[6:7]
	v_cmp_class_f32_e64 s[6:7], v5, v63
	s_nop 1
	v_cndmask_b32_e64 v5, v6, v5, s[6:7]
	v_div_scale_f32 v6, s[6:7], v5, v5, 1.0
	v_rcp_f32_e32 v8, v6
	s_nop 0
	v_fma_f32 v2, -v6, v8, 1.0
	v_fmac_f32_e32 v8, v2, v8
	v_div_scale_f32 v2, vcc, 1.0, v5, 1.0
	v_mul_f32_e32 v3, v2, v8
	v_fma_f32 v4, -v6, v3, v2
	v_fmac_f32_e32 v3, v4, v8
	v_fma_f32 v2, -v6, v3, v2
	v_div_fmas_f32 v2, v2, v8, v3
	v_div_fixup_f32 v2, v2, v5, 1.0
	global_store_dword v65, v2, s[34:35]
	s_branch .LBB0_12

.LBB0_18:
	s_mov_b64 s[6:7], s[0:1]
	s_load_dwordx2 s[6:7], s[6:7], 0x8
	s_waitcnt lgkmcnt(0)
	v_lshl_add_u64 v[48:49], s[6:7], 0, v[4:5]
	v_add_co_u32_e32 v50, vcc, 0xfffff000, v48
	global_load_dwordx4 v[16:19], v[48:49], off offset:-4096 nt
	global_load_dwordx4 v[20:23], v[48:49], off offset:-3072 nt
	global_load_dwordx4 v[24:27], v[48:49], off offset:-2048 nt
	global_load_dwordx4 v[28:31], v[48:49], off offset:-1024 nt
	v_addc_co_u32_e32 v51, vcc, -1, v49, vcc
	global_load_dwordx4 v[32:35], v[50:51], off offset:-3072 nt
	global_load_dwordx4 v[36:39], v[50:51], off offset:-2048 nt
	global_load_dwordx4 v[40:43], v[50:51], off offset:-1024 nt
	global_load_dwordx4 v[44:47], v[48:49], off nt
	v_cmp_lt_i32_e32 vcc, v7, v6
	v_lshl_add_u64 v[48:49], s[82:83], 0, v[2:3]
	s_waitcnt vmcnt(7)
	v_mul_f32_e32 v56, v17, v17
	v_mul_f32_e32 v57, v19, v19
	s_waitcnt vmcnt(6)
	v_mul_f32_e32 v58, v21, v21
	v_mul_f32_e32 v59, v23, v23
	s_waitcnt vmcnt(5)
	v_mul_f32_e32 v60, v25, v25
	v_mul_f32_e32 v61, v27, v27
	s_waitcnt vmcnt(4)
	v_mul_f32_e32 v62, v29, v29
	v_mul_f32_e32 v63, v31, v31
	v_fmac_f32_e32 v56, v16, v16
	v_fmac_f32_e32 v57, v18, v18
	v_fmac_f32_e32 v58, v20, v20
	v_fmac_f32_e32 v59, v22, v22
	v_fmac_f32_e32 v60, v24, v24
	v_fmac_f32_e32 v61, v26, v26
	s_waitcnt vmcnt(3)
	v_mul_f32_e32 v64, v33, v33
	v_mul_f32_e32 v65, v35, v35
	s_waitcnt vmcnt(2)
	v_mul_f32_e32 v66, v37, v37
	v_mul_f32_e32 v67, v39, v39
	v_fmac_f32_e32 v62, v28, v28
	v_fmac_f32_e32 v63, v30, v30
	s_waitcnt vmcnt(1)
	v_mul_f32_e32 v68, v41, v41
	v_mul_f32_e32 v69, v43, v43
	v_add_f32_e32 v56, v56, v57
	v_add_f32_e32 v57, v58, v59
	v_add_f32_e32 v58, v60, v61
	s_waitcnt vmcnt(0)
	v_mul_f32_e32 v60, v45, v45
	v_mul_f32_e32 v61, v47, v47
	v_fmac_f32_e32 v64, v32, v32
	v_fmac_f32_e32 v65, v34, v34
	v_fmac_f32_e32 v66, v36, v36
	v_fmac_f32_e32 v67, v38, v38
	v_add_f32_e32 v59, v62, v63
	v_fmac_f32_e32 v68, v40, v40
	v_fmac_f32_e32 v69, v42, v42
	v_fmac_f32_e32 v60, v44, v44
	v_fmac_f32_e32 v61, v46, v46
	v_add_f32_e32 v62, v64, v65
	v_add_f32_e32 v63, v66, v67
	v_add_f32_e32 v64, v68, v69
	v_add_f32_e32 v60, v60, v61
	v_add_f32_e32 v61, v62, v63
	v_add_f32_e32 v61, v61, v64
	v_add_f32_e32 v56, v61, v56
	v_add_f32_e32 v56, v56, v57
	v_add_f32_e32 v56, v56, v58
	v_cndmask_b32_e32 v50, v1, v7, vcc
	v_add_f32_e32 v56, v56, v59
	v_lshlrev_b32_e32 v50, 2, v50
	v_add_f32_e32 v56, v56, v60
	ds_bpermute_b32 v50, v50, v56
	v_cmp_lt_i32_e32 vcc, v8, v6
	v_cvt_pk_bf16_f32 v16, v16, v17
	v_cvt_pk_bf16_f32 v17, v18, v19
	v_cndmask_b32_e32 v51, v1, v8, vcc
	v_lshlrev_b32_e32 v51, 2, v51
	s_waitcnt lgkmcnt(0)
	v_add_f32_e32 v50, v56, v50
	ds_bpermute_b32 v51, v51, v50
	v_cmp_lt_i32_e32 vcc, v9, v6
	v_cvt_pk_bf16_f32 v19, v22, v23
	v_cvt_pk_bf16_f32 v18, v20, v21
	v_cndmask_b32_e32 v52, v1, v9, vcc
	v_lshlrev_b32_e32 v52, 2, v52
	s_waitcnt lgkmcnt(0)
	v_add_f32_e32 v23, v50, v51
	v_cmp_lt_i32_e32 vcc, v10, v6
	v_cvt_pk_bf16_f32 v20, v24, v25
	ds_bpermute_b32 v24, v52, v23
	v_cndmask_b32_e32 v53, v1, v10, vcc
	v_cmp_lt_i32_e32 vcc, v11, v6
	v_cvt_pk_bf16_f32 v21, v26, v27
	v_lshlrev_b32_e32 v53, 2, v53
	v_cndmask_b32_e32 v54, v1, v11, vcc
	v_cmp_lt_i32_e32 vcc, v12, v6
	v_lshlrev_b32_e32 v54, 2, v54
	v_cvt_pk_bf16_f32 v22, v28, v29
	v_cndmask_b32_e32 v55, v1, v12, vcc
	v_add_co_u32_e32 v48, vcc, s13, v48
	v_lshlrev_b32_e32 v55, 2, v55
	s_nop 0
	v_addc_co_u32_e32 v49, vcc, 0, v49, vcc
	global_store_dwordx2 v[48:49], v[16:17], off offset:1536 nt
	global_store_dwordx2 v[48:49], v[18:19], off offset:2048 nt
	global_store_dwordx2 v[48:49], v[20:21], off offset:2560 nt
	s_waitcnt lgkmcnt(0)
	v_add_f32_e32 v21, v23, v24
	ds_bpermute_b32 v23, v53, v21
	v_cvt_pk_bf16_f32 v16, v32, v33
	v_cvt_pk_bf16_f32 v17, v34, v35
	v_cvt_pk_bf16_f32 v18, v36, v37
	v_cvt_pk_bf16_f32 v19, v38, v39
	s_waitcnt lgkmcnt(0)
	v_add_f32_e32 v23, v21, v23
	ds_bpermute_b32 v24, v54, v23
	v_cvt_pk_bf16_f32 v20, v40, v41
	v_cvt_pk_bf16_f32 v21, v42, v43
	global_store_dwordx2 v[48:49], v[16:17], off nt
	global_store_dwordx2 v[48:49], v[18:19], off offset:512 nt
	global_store_dwordx2 v[48:49], v[20:21], off offset:1024 nt
	v_cvt_pk_bf16_f32 v18, v44, v45
	s_waitcnt lgkmcnt(0)
	v_add_f32_e32 v16, v23, v24
	ds_bpermute_b32 v17, v55, v16
	v_cvt_pk_bf16_f32 v23, v30, v31
	v_cvt_pk_bf16_f32 v19, v46, v47
	global_store_dwordx2 v[48:49], v[22:23], off offset:3072 nt
	global_store_dwordx2 v[48:49], v[18:19], off offset:3584 nt
	s_and_saveexec_b64 s[20:21], s[4:5]
	s_cbranch_execz .LBB0_17
	s_waitcnt lgkmcnt(0)
	v_add_f32_e32 v16, v16, v17
	v_fmamk_f32 v16, v16, 0x3a000000, v14
	v_mul_f32_e32 v17, 0x4f800000, v16
	v_cmp_gt_f32_e32 vcc, s15, v16
	s_nop 1
	v_cndmask_b32_e32 v16, v16, v17, vcc
	v_sqrt_f32_e32 v17, v16
	s_nop 0
	v_add_u32_e32 v18, -1, v17
	v_fma_f32 v20, -v18, v17, v16
	v_add_u32_e32 v19, 1, v17
	v_cmp_ge_f32_e64 s[6:7], 0, v20
	s_nop 1
	v_cndmask_b32_e64 v18, v17, v18, s[6:7]
	v_fma_f32 v17, -v19, v17, v16
	v_cmp_lt_f32_e64 s[6:7], 0, v17
	s_nop 1
	v_cndmask_b32_e64 v17, v18, v19, s[6:7]
	v_mul_f32_e32 v18, 0x37800000, v17
	v_cndmask_b32_e32 v17, v17, v18, vcc
	v_cmp_class_f32_e32 vcc, v16, v15
	s_nop 1
	v_cndmask_b32_e32 v16, v17, v16, vcc
	v_div_scale_f32 v17, s[6:7], v16, v16, 1.0
	v_rcp_f32_e32 v18, v17
	s_add_u32 s6, s82, s3
	s_addc_u32 s7, s83, s22
	v_fma_f32 v19, -v17, v18, 1.0
	v_fmac_f32_e32 v18, v19, v18
	v_div_scale_f32 v19, vcc, 1.0, v16, 1.0
	v_mul_f32_e32 v20, v19, v18
	v_fma_f32 v21, -v17, v20, v19
	v_fmac_f32_e32 v20, v21, v18
	v_fma_f32 v17, -v17, v20, v19
	v_div_fmas_f32 v17, v17, v18, v20
	v_div_fixup_f32 v16, v17, v16, 1.0
	global_store_dword v13, v16, s[6:7]
	s_branch .LBB0_17

.LBB0_165:
	v_mov_b32_e32 v141, v138
	v_mov_b32_e32 v135, v132
	v_pk_mul_f32 v[142:143], v[10:11], v[138:139] op_sel_hi:[1,0]
	v_pk_mul_f32 v[140:141], v[8:9], v[140:141]
	v_pk_mul_f32 v[136:137], v[6:7], v[132:133] op_sel_hi:[1,0]
	v_pk_mul_f32 v[134:135], v[4:5], v[134:135]
	ds_write_b128 v177, v[140:143]
	ds_write_b128 v178, v[134:137]
	s_waitcnt lgkmcnt(0)
	ds_read2st64_b32 v[132:133], v3 offset1:1
	s_cmp_lg_u32 s19, 0
	v_add_u32_e32 v138, s13, v159
	v_add_u32_e32 v137, s13, v161
	v_add_u32_e32 v136, s13, v163
	v_add_u32_e32 v140, s13, v150
	s_cbranch_scc0 .LBB0_178
	ds_read2st64_b32 v[134:135], v3 offset0:2 offset1:3
	s_waitcnt lgkmcnt(1)
	v_max_f32_e32 v141, v132, v132
	v_max_f32_e32 v142, v133, v133
	v_med3_f32 v141, v141, s51, v180
	v_med3_f32 v185, v142, s51, v180
	v_mov_b32_e32 v184, v147
	ds_read2st64_b32 v[142:143], v3 offset0:4 offset1:5
	ds_read2st64_b32 v[182:183], v3 offset0:6 offset1:7
	v_cvt_pk_fp8_f32 v184, v141, v185
	s_waitcnt lgkmcnt(2)
	v_max_f32_e32 v134, v134, v134
	v_max_f32_e32 v135, v135, v135
	v_med3_f32 v134, v134, s51, v180
	v_med3_f32 v135, v135, s51, v180
	v_cvt_pk_fp8_f32 v184, v134, v135 op_sel:[0,0,1]
	s_waitcnt lgkmcnt(1)
	v_max_f32_e32 v134, v142, v142
	v_max_f32_e32 v135, v143, v143
	v_med3_f32 v134, v134, s51, v180
	v_med3_f32 v135, v135, s51, v180
	v_mov_b32_e32 v185, v147
	v_cvt_pk_fp8_f32 v185, v134, v135
	s_waitcnt lgkmcnt(0)
	v_max_f32_e32 v141, v182, v182
	v_max_f32_e32 v135, v183, v183
	v_med3_f32 v134, v141, s51, v180
	v_med3_f32 v135, v135, s51, v180
	v_cvt_pk_fp8_f32 v185, v134, v135 op_sel:[0,0,1]
	v_mov_b64_e32 v[134:135], s[6:7]
	v_mad_u64_u32 v[142:143], s[4:5], s3, v150, v[134:135]
	s_ashr_i32 s17, s16, 31
	v_lshl_add_u64 v[142:143], v[142:143], 0, s[16:17]
	ds_read2st64_b32 v[182:183], v139 offset1:1
	v_lshl_add_u64 v[142:143], v[142:143], 0, v[152:153]
	global_store_dwordx2 v[142:143], v[184:185], off nt
	ds_read2st64_b32 v[142:143], v139 offset0:2 offset1:3
	ds_read2st64_b32 v[184:185], v139 offset0:4 offset1:5
	ds_read2st64_b32 v[186:187], v139 offset0:6 offset1:7
	s_waitcnt lgkmcnt(3)
	v_max_f32_e32 v141, v182, v182
	v_max_f32_e32 v182, v183, v183
	v_med3_f32 v141, v141, s51, v180
	v_med3_f32 v182, v182, s51, v180
	s_waitcnt lgkmcnt(2)
	v_max_f32_e32 v183, v142, v142
	v_mov_b32_e32 v142, v147
	v_cvt_pk_fp8_f32 v142, v141, v182
	v_max_f32_e32 v143, v143, v143
	v_med3_f32 v141, v183, s51, v180
	v_med3_f32 v143, v143, s51, v180
	v_cvt_pk_fp8_f32 v142, v141, v143 op_sel:[0,0,1]
	s_waitcnt lgkmcnt(1)
	v_max_f32_e32 v141, v184, v184
	v_max_f32_e32 v143, v185, v185
	v_med3_f32 v141, v141, s51, v180
	v_med3_f32 v182, v143, s51, v180
	v_mov_b32_e32 v143, v147
	v_cvt_pk_fp8_f32 v143, v141, v182
	s_waitcnt lgkmcnt(0)
	v_max_f32_e32 v183, v186, v186
	v_max_f32_e32 v182, v187, v187
	v_med3_f32 v141, v183, s51, v180
	v_med3_f32 v182, v182, s51, v180
	v_cvt_pk_fp8_f32 v143, v141, v182 op_sel:[0,0,1]
	v_mad_u64_u32 v[182:183], s[4:5], s3, v154, v[134:135]
	v_lshl_add_u64 v[182:183], v[182:183], 0, s[16:17]
	ds_read2st64_b32 v[184:185], v149 offset1:1
	v_lshl_add_u64 v[182:183], v[182:183], 0, v[152:153]
	global_store_dwordx2 v[182:183], v[142:143], off nt
	ds_read2st64_b32 v[142:143], v149 offset0:2 offset1:3
	ds_read2st64_b32 v[182:183], v149 offset0:4 offset1:5
	ds_read2st64_b32 v[186:187], v149 offset0:6 offset1:7
	s_waitcnt lgkmcnt(3)
	v_max_f32_e32 v141, v184, v184
	v_max_f32_e32 v184, v185, v185
	v_med3_f32 v141, v141, s51, v180
	v_med3_f32 v184, v184, s51, v180
	s_waitcnt lgkmcnt(2)
	v_max_f32_e32 v185, v142, v142
	v_mov_b32_e32 v142, v147
	v_cvt_pk_fp8_f32 v142, v141, v184
	v_max_f32_e32 v143, v143, v143
	v_med3_f32 v141, v185, s51, v180
	v_med3_f32 v143, v143, s51, v180
	v_cvt_pk_fp8_f32 v142, v141, v143 op_sel:[0,0,1]
	s_waitcnt lgkmcnt(1)
	v_max_f32_e32 v141, v182, v182
	v_max_f32_e32 v143, v183, v183
	v_med3_f32 v141, v141, s51, v180
	v_med3_f32 v182, v143, s51, v180
	v_mov_b32_e32 v143, v147
	v_cvt_pk_fp8_f32 v143, v141, v182
	s_waitcnt lgkmcnt(0)
	v_max_f32_e32 v183, v186, v186
	v_max_f32_e32 v182, v187, v187
	v_med3_f32 v141, v183, s51, v180
	v_med3_f32 v182, v182, s51, v180
	v_cvt_pk_fp8_f32 v143, v141, v182 op_sel:[0,0,1]
	v_mad_u64_u32 v[182:183], s[4:5], s3, v156, v[134:135]
	v_lshl_add_u64 v[182:183], v[182:183], 0, s[16:17]
	ds_read2st64_b32 v[184:185], v151 offset1:1
	v_lshl_add_u64 v[182:183], v[182:183], 0, v[152:153]
	global_store_dwordx2 v[182:183], v[142:143], off nt
	ds_read2st64_b32 v[142:143], v151 offset0:2 offset1:3
	ds_read2st64_b32 v[182:183], v151 offset0:4 offset1:5
	ds_read2st64_b32 v[186:187], v151 offset0:6 offset1:7
	s_waitcnt lgkmcnt(3)
	v_max_f32_e32 v141, v184, v184
	v_max_f32_e32 v184, v185, v185
	v_med3_f32 v141, v141, s51, v180
	v_med3_f32 v184, v184, s51, v180
	s_waitcnt lgkmcnt(2)
	v_max_f32_e32 v185, v142, v142
	v_mov_b32_e32 v142, v147
	v_cvt_pk_fp8_f32 v142, v141, v184
	v_max_f32_e32 v143, v143, v143
	v_med3_f32 v141, v185, s51, v180
	v_med3_f32 v143, v143, s51, v180
	v_cvt_pk_fp8_f32 v142, v141, v143 op_sel:[0,0,1]
	s_waitcnt lgkmcnt(1)
	v_max_f32_e32 v141, v182, v182
	v_max_f32_e32 v143, v183, v183
	v_med3_f32 v141, v141, s51, v180
	v_med3_f32 v182, v143, s51, v180
	v_mov_b32_e32 v143, v147
	v_cvt_pk_fp8_f32 v143, v141, v182
	s_waitcnt lgkmcnt(0)
	v_max_f32_e32 v183, v186, v186
	v_max_f32_e32 v182, v187, v187
	v_med3_f32 v141, v183, s51, v180
	v_med3_f32 v182, v182, s51, v180
	v_cvt_pk_fp8_f32 v143, v141, v182 op_sel:[0,0,1]
	v_mad_u64_u32 v[182:183], s[4:5], s3, v158, v[134:135]
	v_lshl_add_u64 v[182:183], v[182:183], 0, s[16:17]
	ds_read2st64_b32 v[184:185], v155 offset1:1
	v_lshl_add_u64 v[182:183], v[182:183], 0, v[152:153]
	global_store_dwordx2 v[182:183], v[142:143], off nt
	ds_read2st64_b32 v[142:143], v155 offset0:2 offset1:3
	ds_read2st64_b32 v[182:183], v155 offset0:4 offset1:5
	ds_read2st64_b32 v[186:187], v155 offset0:6 offset1:7
	s_waitcnt lgkmcnt(3)
	v_max_f32_e32 v141, v184, v184
	v_max_f32_e32 v184, v185, v185
	v_med3_f32 v141, v141, s51, v180
	v_med3_f32 v184, v184, s51, v180
	s_waitcnt lgkmcnt(2)
	v_max_f32_e32 v185, v142, v142
	v_mov_b32_e32 v142, v147
	v_cvt_pk_fp8_f32 v142, v141, v184
	v_max_f32_e32 v143, v143, v143
	v_med3_f32 v141, v185, s51, v180
	v_med3_f32 v143, v143, s51, v180
	v_cvt_pk_fp8_f32 v142, v141, v143 op_sel:[0,0,1]
	s_waitcnt lgkmcnt(1)
	v_max_f32_e32 v141, v182, v182
	v_max_f32_e32 v143, v183, v183
	v_med3_f32 v141, v141, s51, v180
	v_med3_f32 v182, v143, s51, v180
	v_mov_b32_e32 v143, v147
	v_cvt_pk_fp8_f32 v143, v141, v182
	s_waitcnt lgkmcnt(0)
	v_max_f32_e32 v183, v186, v186
	v_max_f32_e32 v182, v187, v187
	v_med3_f32 v141, v183, s51, v180
	v_med3_f32 v182, v182, s51, v180
	v_cvt_pk_fp8_f32 v143, v141, v182 op_sel:[0,0,1]
	v_mad_u64_u32 v[182:183], s[4:5], v140, s3, v[134:135]
	v_lshl_add_u64 v[182:183], v[182:183], 0, s[16:17]
	ds_read2st64_b32 v[184:185], v157 offset1:1
	v_lshl_add_u64 v[182:183], v[182:183], 0, v[152:153]
	global_store_dwordx2 v[182:183], v[142:143], off nt
	ds_read2st64_b32 v[142:143], v157 offset0:2 offset1:3
	ds_read2st64_b32 v[182:183], v157 offset0:4 offset1:5
	ds_read2st64_b32 v[186:187], v157 offset0:6 offset1:7
	s_waitcnt lgkmcnt(3)
	v_max_f32_e32 v141, v184, v184
	v_max_f32_e32 v184, v185, v185
	v_med3_f32 v141, v141, s51, v180
	v_med3_f32 v184, v184, s51, v180
	s_waitcnt lgkmcnt(2)
	v_max_f32_e32 v185, v142, v142
	v_mov_b32_e32 v142, v147
	v_cvt_pk_fp8_f32 v142, v141, v184
	v_max_f32_e32 v143, v143, v143
	v_med3_f32 v141, v185, s51, v180
	v_med3_f32 v143, v143, s51, v180
	v_cvt_pk_fp8_f32 v142, v141, v143 op_sel:[0,0,1]
	s_waitcnt lgkmcnt(1)
	v_max_f32_e32 v141, v182, v182
	v_max_f32_e32 v143, v183, v183
	v_med3_f32 v141, v141, s51, v180
	v_med3_f32 v182, v143, s51, v180
	v_mov_b32_e32 v143, v147
	v_cvt_pk_fp8_f32 v143, v141, v182
	s_waitcnt lgkmcnt(0)
	v_max_f32_e32 v183, v186, v186
	v_max_f32_e32 v182, v187, v187
	v_med3_f32 v141, v183, s51, v180
	v_med3_f32 v182, v182, s51, v180
	v_cvt_pk_fp8_f32 v143, v141, v182 op_sel:[0,0,1]
	v_mad_u64_u32 v[182:183], s[4:5], v138, s3, v[134:135]
	v_lshl_add_u64 v[182:183], v[182:183], 0, s[16:17]
	ds_read2st64_b32 v[184:185], v160 offset1:1
	v_lshl_add_u64 v[182:183], v[182:183], 0, v[152:153]
	global_store_dwordx2 v[182:183], v[142:143], off nt
	ds_read2st64_b32 v[142:143], v160 offset0:2 offset1:3
	ds_read2st64_b32 v[182:183], v160 offset0:4 offset1:5
	ds_read2st64_b32 v[186:187], v160 offset0:6 offset1:7
	s_waitcnt lgkmcnt(3)
	v_max_f32_e32 v141, v184, v184
	v_max_f32_e32 v184, v185, v185
	v_med3_f32 v141, v141, s51, v180
	v_med3_f32 v184, v184, s51, v180
	s_waitcnt lgkmcnt(2)
	v_max_f32_e32 v185, v142, v142
	v_mov_b32_e32 v142, v147
	v_cvt_pk_fp8_f32 v142, v141, v184
	v_max_f32_e32 v143, v143, v143
	v_med3_f32 v141, v185, s51, v180
	v_med3_f32 v143, v143, s51, v180
	v_cvt_pk_fp8_f32 v142, v141, v143 op_sel:[0,0,1]
	s_waitcnt lgkmcnt(1)
	v_max_f32_e32 v141, v182, v182
	v_max_f32_e32 v143, v183, v183
	v_med3_f32 v141, v141, s51, v180
	v_med3_f32 v182, v143, s51, v180
	v_mov_b32_e32 v143, v147
	v_cvt_pk_fp8_f32 v143, v141, v182
	s_waitcnt lgkmcnt(0)
	v_max_f32_e32 v183, v186, v186
	v_max_f32_e32 v182, v187, v187
	v_med3_f32 v141, v183, s51, v180
	v_med3_f32 v182, v182, s51, v180
	v_cvt_pk_fp8_f32 v143, v141, v182 op_sel:[0,0,1]
	v_mad_u64_u32 v[182:183], s[4:5], v137, s3, v[134:135]
	v_lshl_add_u64 v[182:183], v[182:183], 0, s[16:17]
	ds_read2st64_b32 v[184:185], v162 offset1:1
	v_lshl_add_u64 v[182:183], v[182:183], 0, v[152:153]
	global_store_dwordx2 v[182:183], v[142:143], off nt
	ds_read2st64_b32 v[142:143], v162 offset0:2 offset1:3
	ds_read2st64_b32 v[182:183], v162 offset0:4 offset1:5
	ds_read2st64_b32 v[186:187], v162 offset0:6 offset1:7
	v_mad_u64_u32 v[134:135], s[4:5], v136, s3, v[134:135]
	s_waitcnt lgkmcnt(3)
	v_max_f32_e32 v141, v184, v184
	v_max_f32_e32 v184, v185, v185
	v_med3_f32 v141, v141, s51, v180
	v_med3_f32 v184, v184, s51, v180
	s_waitcnt lgkmcnt(2)
	v_max_f32_e32 v185, v142, v142
	v_mov_b32_e32 v142, v147
	v_cvt_pk_fp8_f32 v142, v141, v184
	v_max_f32_e32 v143, v143, v143
	v_med3_f32 v141, v185, s51, v180
	v_med3_f32 v143, v143, s51, v180
	v_cvt_pk_fp8_f32 v142, v141, v143 op_sel:[0,0,1]
	s_waitcnt lgkmcnt(1)
	v_max_f32_e32 v141, v182, v182
	v_max_f32_e32 v143, v183, v183
	v_med3_f32 v141, v141, s51, v180
	v_med3_f32 v182, v143, s51, v180
	v_mov_b32_e32 v143, v147
	v_cvt_pk_fp8_f32 v143, v141, v182
	s_waitcnt lgkmcnt(0)
	v_max_f32_e32 v183, v186, v186
	v_max_f32_e32 v182, v187, v187
	v_med3_f32 v141, v183, s51, v180
	v_med3_f32 v182, v182, s51, v180
	v_cvt_pk_fp8_f32 v143, v141, v182 op_sel:[0,0,1]
	v_lshl_add_u64 v[134:135], v[134:135], 0, s[16:17]
	v_lshl_add_u64 v[134:135], v[134:135], 0, v[152:153]
	global_store_dwordx2 v[134:135], v[142:143], off nt
	s_cbranch_execnz .LBB0_168
.LBB0_167:
	ds_read2st64_b32 v[134:135], v3 offset0:2 offset1:3
	ds_read2st64_b32 v[142:143], v3 offset0:4 offset1:5
	ds_read2st64_b32 v[182:183], v3 offset0:6 offset1:7
	s_ashr_i32 s17, s16, 31
	ds_read2st64_b32 v[184:185], v139 offset1:1
	ds_read2st64_b32 v[186:187], v139 offset0:2 offset1:3
	ds_read2st64_b32 v[188:189], v139 offset0:4 offset1:5
	ds_read2st64_b32 v[190:191], v139 offset0:6 offset1:7
	s_waitcnt lgkmcnt(7)
	v_cvt_pk_bf16_f32 v132, v132, v133
	s_waitcnt lgkmcnt(6)
	v_cvt_pk_bf16_f32 v133, v134, v135
	s_waitcnt lgkmcnt(5)
	v_cvt_pk_bf16_f32 v134, v142, v143
	v_lshl_add_u64 v[142:143], s[16:17], 0, v[152:153]
	s_waitcnt lgkmcnt(4)
	v_cvt_pk_bf16_f32 v135, v182, v183
	v_mad_u64_u32 v[182:183], s[4:5], s3, v150, v[142:143]
	v_lshl_add_u64 v[182:183], v[182:183], 1, s[6:7]
	global_store_dwordx4 v[182:183], v[132:135], off nt
	v_mad_u64_u32 v[182:183], s[4:5], s3, v154, v[142:143]
	s_waitcnt lgkmcnt(3)
	v_cvt_pk_bf16_f32 v132, v184, v185
	s_waitcnt lgkmcnt(2)
	v_cvt_pk_bf16_f32 v133, v186, v187
	s_waitcnt lgkmcnt(1)
	v_cvt_pk_bf16_f32 v134, v188, v189
	s_waitcnt lgkmcnt(0)
	v_cvt_pk_bf16_f32 v135, v190, v191
	ds_read2st64_b32 v[184:185], v149 offset1:1
	ds_read2st64_b32 v[186:187], v149 offset0:2 offset1:3
	ds_read2st64_b32 v[188:189], v149 offset0:4 offset1:5
	ds_read2st64_b32 v[190:191], v149 offset0:6 offset1:7
	v_lshl_add_u64 v[182:183], v[182:183], 1, s[6:7]
	global_store_dwordx4 v[182:183], v[132:135], off nt
	v_mad_u64_u32 v[182:183], s[4:5], s3, v156, v[142:143]
	s_waitcnt lgkmcnt(3)
	v_cvt_pk_bf16_f32 v132, v184, v185
	s_waitcnt lgkmcnt(2)
	v_cvt_pk_bf16_f32 v133, v186, v187
	s_waitcnt lgkmcnt(1)
	v_cvt_pk_bf16_f32 v134, v188, v189
	s_waitcnt lgkmcnt(0)
	v_cvt_pk_bf16_f32 v135, v190, v191
	ds_read2st64_b32 v[184:185], v151 offset1:1
	ds_read2st64_b32 v[186:187], v151 offset0:2 offset1:3
	ds_read2st64_b32 v[188:189], v151 offset0:4 offset1:5
	ds_read2st64_b32 v[190:191], v151 offset0:6 offset1:7
	v_lshl_add_u64 v[182:183], v[182:183], 1, s[6:7]
	global_store_dwordx4 v[182:183], v[132:135], off nt
	v_mad_u64_u32 v[182:183], s[4:5], s3, v158, v[142:143]
	s_waitcnt lgkmcnt(3)
	v_cvt_pk_bf16_f32 v132, v184, v185
	s_waitcnt lgkmcnt(2)
	v_cvt_pk_bf16_f32 v133, v186, v187
	s_waitcnt lgkmcnt(1)
	v_cvt_pk_bf16_f32 v134, v188, v189
	s_waitcnt lgkmcnt(0)
	v_cvt_pk_bf16_f32 v135, v190, v191
	ds_read2st64_b32 v[184:185], v155 offset1:1
	ds_read2st64_b32 v[186:187], v155 offset0:2 offset1:3
	ds_read2st64_b32 v[188:189], v155 offset0:4 offset1:5
	ds_read2st64_b32 v[190:191], v155 offset0:6 offset1:7
	v_lshl_add_u64 v[182:183], v[182:183], 1, s[6:7]
	global_store_dwordx4 v[182:183], v[132:135], off nt
	v_mad_u64_u32 v[140:141], s[4:5], v140, s3, v[142:143]
	s_waitcnt lgkmcnt(3)
	v_cvt_pk_bf16_f32 v132, v184, v185
	s_waitcnt lgkmcnt(2)
	v_cvt_pk_bf16_f32 v133, v186, v187
	s_waitcnt lgkmcnt(1)
	v_cvt_pk_bf16_f32 v134, v188, v189
	ds_read2st64_b32 v[182:183], v157 offset1:1
	ds_read2st64_b32 v[184:185], v157 offset0:2 offset1:3
	ds_read2st64_b32 v[186:187], v157 offset0:4 offset1:5
	ds_read2st64_b32 v[188:189], v157 offset0:6 offset1:7
	s_waitcnt lgkmcnt(4)
	v_cvt_pk_bf16_f32 v135, v190, v191
	v_lshl_add_u64 v[140:141], v[140:141], 1, s[6:7]
	global_store_dwordx4 v[140:141], v[132:135], off nt
	v_mad_u64_u32 v[140:141], s[4:5], v138, s3, v[142:143]
	s_waitcnt lgkmcnt(3)
	v_cvt_pk_bf16_f32 v132, v182, v183
	s_waitcnt lgkmcnt(2)
	v_cvt_pk_bf16_f32 v133, v184, v185
	s_waitcnt lgkmcnt(1)
	v_cvt_pk_bf16_f32 v134, v186, v187
	s_waitcnt lgkmcnt(0)
	v_cvt_pk_bf16_f32 v135, v188, v189
	ds_read2st64_b32 v[182:183], v160 offset1:1
	ds_read2st64_b32 v[184:185], v160 offset0:2 offset1:3
	ds_read2st64_b32 v[186:187], v160 offset0:4 offset1:5
	ds_read2st64_b32 v[188:189], v160 offset0:6 offset1:7
	v_lshl_add_u64 v[140:141], v[140:141], 1, s[6:7]
	global_store_dwordx4 v[140:141], v[132:135], off nt
	v_mad_u64_u32 v[140:141], s[4:5], v137, s3, v[142:143]
	s_waitcnt lgkmcnt(3)
	v_cvt_pk_bf16_f32 v132, v182, v183
	s_waitcnt lgkmcnt(2)
	v_cvt_pk_bf16_f32 v133, v184, v185
	s_waitcnt lgkmcnt(1)
	v_cvt_pk_bf16_f32 v134, v186, v187
	s_waitcnt lgkmcnt(0)
	v_cvt_pk_bf16_f32 v135, v188, v189
	ds_read2st64_b32 v[182:183], v162 offset1:1
	ds_read2st64_b32 v[184:185], v162 offset0:2 offset1:3
	ds_read2st64_b32 v[186:187], v162 offset0:4 offset1:5
	ds_read2st64_b32 v[188:189], v162 offset0:6 offset1:7
	v_lshl_add_u64 v[140:141], v[140:141], 1, s[6:7]
	v_mad_u64_u32 v[136:137], s[4:5], v136, s3, v[142:143]
	global_store_dwordx4 v[140:141], v[132:135], off nt
	v_lshl_add_u64 v[136:137], v[136:137], 1, s[6:7]
	s_waitcnt lgkmcnt(3)
	v_cvt_pk_bf16_f32 v132, v182, v183
	s_waitcnt lgkmcnt(2)
	v_cvt_pk_bf16_f32 v133, v184, v185
	s_waitcnt lgkmcnt(1)
	v_cvt_pk_bf16_f32 v134, v186, v187
	s_waitcnt lgkmcnt(0)
	v_cvt_pk_bf16_f32 v135, v188, v189
	global_store_dwordx4 v[136:137], v[132:135], off nt

.LBB0_1078:
	s_or_b64 exec, exec, s[6:7]
	s_lshl_b32 s3, s87, 3
	s_add_i32 s10, s3, s88
	s_cmpk_gt_i32 s10, 0x7fff
	s_waitcnt lgkmcnt(0)
	s_barrier
	s_cbranch_scc1 .LBB0_1085
	s_add_u32 s12, s82, 0x57e00000
	s_addc_u32 s13, s83, 0
	s_add_u32 s3, s82, 0x2300000
	s_addc_u32 s19, s83, 0
	s_lshl_b32 s4, s10, 1
	s_ashr_i32 s5, s4, 31
	s_lshl_b32 s14, s84, 3
	s_lshl_b64 s[4:5], s[4:5], 2
	s_add_u32 s4, s3, s4
	v_mov_b32_e32 v1, 0
	s_addc_u32 s5, s19, s5
	global_load_dwordx2 v[2:3], v1, s[4:5] nt
	v_mbcnt_lo_u32_b32 v4, -1, 0
	v_mbcnt_hi_u32_b32 v4, -1, v4
	v_and_b32_e32 v5, 64, v4
	v_xor_b32_e32 v6, 1, v4
	v_add_u32_e32 v5, 64, v5
	v_xor_b32_e32 v7, 2, v4
	v_cmp_lt_i32_e32 vcc, v6, v5
	v_xor_b32_e32 v8, 4, v4
	v_xor_b32_e32 v9, 8, v4
	v_cndmask_b32_e32 v6, v4, v6, vcc
	v_cmp_lt_i32_e32 vcc, v7, v5
	s_add_i32 s15, s10, s14
	s_ashr_i32 s11, s10, 31
	v_cndmask_b32_e32 v7, v4, v7, vcc
	v_cmp_lt_i32_e32 vcc, v8, v5
	v_xor_b32_e32 v10, 16, v4
	s_lshl_b32 s37, s84, 4
	v_cndmask_b32_e32 v8, v4, v8, vcc
	v_cmp_lt_i32_e32 vcc, v9, v5
	s_lshl_b32 s20, s15, 1
	s_lshl_b64 s[22:23], s[10:11], 2
	v_xor_b32_e32 v11, 32, v4
	v_cndmask_b32_e32 v9, v4, v9, vcc
	v_cmp_lt_i32_e32 vcc, v10, v5
	s_add_u32 s38, s22, 0x140000
	s_addc_u32 s39, s23, 0
	v_cndmask_b32_e32 v10, v4, v10, vcc
	v_cmp_lt_i32_e32 vcc, v11, v5
	s_lshl_b64 s[24:25], s[10:11], 12
	s_mov_b64 s[6:7], 0x46c00000
	v_cndmask_b32_e32 v4, v4, v11, vcc
	s_ashr_i32 s15, s14, 31
	s_lshl_b64 s[26:27], s[10:11], 11
	v_lshl_or_b32 v18, v246, 4, s24
	v_mov_b32_e32 v19, s25
	s_mov_b32 s17, 0
	v_cmp_eq_u32_e64 s[4:5], 0, v246
	v_lshlrev_b32_e32 v40, 3, v246
	s_mov_b32 s18, 0x3c800000
	s_mov_b32 s33, 0x36800000
	s_mov_b32 s34, 0xc3e00000
	s_mov_b32 s35, 0x6ee00000
	v_mov_b32_e32 v41, 0x358637bd
	s_mov_b32 s36, 0xf800000
	v_mov_b32_e32 v42, 0x260
	v_lshlrev_b32_e32 v43, 2, v6
	v_lshlrev_b32_e32 v44, 2, v7
	v_lshlrev_b32_e32 v45, 2, v8
	v_lshlrev_b32_e32 v46, 2, v9
	v_lshlrev_b32_e32 v47, 2, v10
	v_lshlrev_b32_e32 v48, 2, v4
	s_add_i32 s11, 0, 0x23c80
	s_lshl_b64 s[22:23], s[14:15], 2
	s_lshl_b64 s[24:25], s[14:15], 12
	v_lshl_or_b32 v20, v246, 3, s26
	v_mov_b32_e32 v21, s27
	s_lshl_b64 s[26:27], s[14:15], 11
	v_lshl_add_u64 v[22:23], v[18:19], 0, s[6:7]
	v_mov_b32_e32 v49, 0x43e00000
	s_waitcnt vmcnt(0)
	v_readfirstlane_b32 s15, v2
	v_readfirstlane_b32 s21, v3
	s_branch .LBB0_1081

.LBB0_1081:
	s_ashr_i32 s6, s15, 16
	s_lshl_b32 s6, s6, 2
	s_add_i32 s6, s11, s6
	v_mov_b32_e32 v2, s6
	s_ashr_i32 s6, s21, 16
	s_lshl_b32 s6, s6, 2
	s_add_i32 s6, s11, s6
	s_waitcnt lgkmcnt(0)
	v_mov_b32_e32 v3, s6
	ds_read_b32 v2, v2
	ds_read_b32 v4, v3
	s_lshl_b32 s6, s15, 11
	s_and_b32 s16, s6, 0x7fff800
	s_lshl_b32 s6, s21, 11
	s_waitcnt lgkmcnt(1)
	v_ashrrev_i32_e32 v3, 31, v2
	s_waitcnt lgkmcnt(0)
	v_ashrrev_i32_e32 v5, 31, v4
	v_lshlrev_b64 v[2:3], 19, v[2:3]
	v_lshl_add_u64 v[2:3], s[12:13], 0, v[2:3]
	v_lshlrev_b64 v[4:5], 19, v[4:5]
	v_lshl_add_u64 v[2:3], v[2:3], 0, s[16:17]
	s_and_b32 s16, s6, 0x7fff800
	v_lshl_add_u64 v[4:5], s[12:13], 0, v[4:5]
	v_lshl_add_u64 v[24:25], s[82:83], 0, v[22:23]
	v_lshl_add_u64 v[4:5], v[4:5], 0, s[16:17]
	v_readfirstlane_b32 s6, v2
	v_readfirstlane_b32 s7, v3
	v_readfirstlane_b32 s28, v4
	v_readfirstlane_b32 s29, v5
	global_load_dwordx4 v[14:17], v[24:25], off nt
	global_load_dwordx4 v[10:13], v[24:25], off offset:1024 nt
	global_load_dwordx4 v[6:9], v[24:25], off offset:2048 nt
	global_load_dwordx4 v[2:5], v[24:25], off offset:3072 nt
	global_load_dwordx2 v[36:37], v40, s[6:7] nt
	global_load_dwordx2 v[32:33], v40, s[6:7] offset:512 nt
	global_load_dwordx2 v[28:29], v40, s[6:7] offset:1024 nt
	s_nop 0
	global_load_dwordx2 v[24:25], v40, s[6:7] offset:1536 nt
	global_load_dwordx2 v[38:39], v40, s[28:29] nt
	global_load_dwordx2 v[34:35], v40, s[28:29] offset:512 nt
	global_load_dwordx2 v[30:31], v40, s[28:29] offset:1024 nt
	global_load_dwordx2 v[26:27], v40, s[28:29] offset:1536 nt
	s_add_i32 s10, s10, s14
	s_cmpk_gt_i32 s10, 0x7fff
	s_cselect_b64 s[28:29], -1, 0
	s_and_b64 vcc, exec, s[28:29]
	s_cbranch_vccnz .LBB0_1083
	s_ashr_i32 s21, s20, 31
	s_lshl_b64 s[6:7], s[20:21], 2
	s_add_u32 s6, s3, s6
	s_addc_u32 s7, s19, s7
	global_load_dwordx2 v[50:51], v1, s[6:7] nt
	s_waitcnt vmcnt(0)
	v_readfirstlane_b32 s15, v50
	v_readfirstlane_b32 s21, v51
.LBB0_1083:
	s_waitcnt vmcnt(7)
	v_cvt_pk_f32_fp8_e32 v[52:53], v36
	v_cvt_pk_f32_fp8_sdwa v[54:55], v36 src0_sel:WORD_1
	s_waitcnt vmcnt(3)
	v_cvt_pk_f32_fp8_e32 v[58:59], v38
	v_cvt_pk_f32_fp8_sdwa v[60:61], v38 src0_sel:WORD_1
	v_cvt_pk_f32_fp8_e32 v[56:57], v37
	v_cvt_pk_f32_fp8_e32 v[62:63], v39
	v_cvt_pk_f32_fp8_sdwa v[36:37], v37 src0_sel:WORD_1
	v_cvt_pk_f32_fp8_sdwa v[38:39], v39 src0_sel:WORD_1
	v_lshlrev_b32_e32 v64, 16, v14
	v_and_b32_e32 v65, 0xffff0000, v14
	v_pk_add_f32 v[52:53], v[52:53], v[58:59]
	v_lshlrev_b32_e32 v14, 16, v15
	v_and_b32_e32 v15, 0xffff0000, v15
	v_pk_add_f32 v[54:55], v[54:55], v[60:61]
	v_pk_fma_f32 v[52:53], v[52:53], s[18:19], v[64:65] op_sel_hi:[1,0,1]
	v_pk_fma_f32 v[54:55], v[54:55], s[18:19], v[14:15] op_sel_hi:[1,0,1]
	v_lshlrev_b32_e32 v14, 16, v16
	v_and_b32_e32 v15, 0xffff0000, v16
	v_pk_add_f32 v[56:57], v[56:57], v[62:63]
	v_lshl_add_u64 v[50:51], s[82:83], 0, v[18:19]
	v_pk_fma_f32 v[56:57], v[56:57], s[18:19], v[14:15] op_sel_hi:[1,0,1]
	v_lshlrev_b32_e32 v14, 16, v17
	v_and_b32_e32 v15, 0xffff0000, v17
	v_pk_add_f32 v[16:17], v[36:37], v[38:39]
	v_cvt_pk_bf16_f32 v36, v52, v53
	v_pk_fma_f32 v[16:17], v[16:17], s[18:19], v[14:15] op_sel_hi:[1,0,1]
	v_cvt_pk_bf16_f32 v37, v54, v55
	v_and_b32_e32 v15, 0xffff0000, v36
	v_lshlrev_b32_e32 v14, 16, v36
	v_mul_f32_e32 v15, v15, v15
	v_and_b32_e32 v58, 0xffff0000, v37
	v_fmac_f32_e32 v15, v14, v14
	v_lshlrev_b32_e32 v14, 16, v37
	v_mul_f32_e32 v58, v58, v58
	v_cvt_pk_bf16_f32 v38, v56, v57
	v_fmac_f32_e32 v58, v14, v14
	v_add_f32_e32 v14, v15, v58
	v_and_b32_e32 v58, 0xffff0000, v38
	v_lshlrev_b32_e32 v15, 16, v38
	v_mul_f32_e32 v58, v58, v58
	v_cvt_pk_bf16_f32 v39, v16, v17
	v_fmac_f32_e32 v58, v15, v15
	v_add_f32_e32 v14, v14, v58
	v_and_b32_e32 v58, 0xffff0000, v39
	v_lshlrev_b32_e32 v15, 16, v39
	v_mul_f32_e32 v58, v58, v58
	v_fmac_f32_e32 v58, v15, v15
	v_add_f32_e32 v60, v14, v58
	v_add_co_u32_e32 v14, vcc, s33, v50
	v_mul_f32_e32 v16, 4.0, v16
	s_nop 0
	v_addc_co_u32_e32 v15, vcc, 0, v51, vcc
	global_store_dwordx4 v[14:15], v[36:39], off nt
	v_mul_f32_e32 v17, 4.0, v17
	v_med3_f32 v16, v16, s34, v49
	v_mul_f32_e32 v36, 4.0, v52
	v_mul_f32_e32 v37, 4.0, v53
	v_med3_f32 v39, v36, s34, v49
	v_med3_f32 v37, v37, s34, v49
	v_mov_b32_e32 v36, 0
	v_cvt_pk_fp8_f32 v36, v39, v37
	v_mul_f32_e32 v38, 4.0, v54
	v_mul_f32_e32 v37, 4.0, v55
	v_med3_f32 v38, v38, s34, v49
	v_med3_f32 v37, v37, s34, v49
	v_cvt_pk_fp8_f32 v36, v38, v37 op_sel:[0,0,1]
	v_mul_f32_e32 v37, 4.0, v56
	v_mul_f32_e32 v38, 4.0, v57
	v_med3_f32 v39, v37, s34, v49
	v_med3_f32 v38, v38, s34, v49
	v_mov_b32_e32 v37, 0
	v_cvt_pk_fp8_f32 v37, v39, v38
	v_med3_f32 v17, v17, s34, v49
	v_cvt_pk_f32_fp8_sdwa v[38:39], v32 src0_sel:WORD_1
	s_waitcnt vmcnt(3)
	v_cvt_pk_f32_fp8_sdwa v[54:55], v34 src0_sel:WORD_1
	v_cvt_pk_fp8_f32 v37, v16, v17 op_sel:[0,0,1]
	v_lshl_add_u64 v[16:17], s[82:83], 0, v[20:21]
	v_add_co_u32_e32 v16, vcc, s35, v16
	v_cvt_pk_f32_fp8_e32 v[50:51], v33
	s_nop 0
	v_addc_co_u32_e32 v17, vcc, 0, v17, vcc
	global_store_dwordx2 v[16:17], v[36:37], off
	v_cvt_pk_f32_fp8_e32 v[36:37], v32
	v_cvt_pk_f32_fp8_e32 v[52:53], v34
	v_cvt_pk_f32_fp8_e32 v[56:57], v35
	v_cvt_pk_f32_fp8_sdwa v[32:33], v33 src0_sel:WORD_1
	v_cvt_pk_f32_fp8_sdwa v[34:35], v35 src0_sel:WORD_1
	v_lshlrev_b32_e32 v58, 16, v10
	v_and_b32_e32 v59, 0xffff0000, v10
	v_lshlrev_b32_e32 v10, 16, v11
	v_and_b32_e32 v11, 0xffff0000, v11
	v_pk_add_f32 v[38:39], v[38:39], v[54:55]
	v_pk_add_f32 v[36:37], v[36:37], v[52:53]
	v_pk_fma_f32 v[38:39], v[38:39], s[18:19], v[10:11] op_sel_hi:[1,0,1]
	v_lshlrev_b32_e32 v10, 16, v12
	v_and_b32_e32 v11, 0xffff0000, v12
	v_pk_add_f32 v[50:51], v[50:51], v[56:57]
	v_pk_fma_f32 v[36:37], v[36:37], s[18:19], v[58:59] op_sel_hi:[1,0,1]
	v_pk_fma_f32 v[50:51], v[50:51], s[18:19], v[10:11] op_sel_hi:[1,0,1]
	v_lshlrev_b32_e32 v10, 16, v13
	v_and_b32_e32 v11, 0xffff0000, v13
	v_pk_add_f32 v[12:13], v[32:33], v[34:35]
	s_nop 0
	v_pk_fma_f32 v[32:33], v[12:13], s[18:19], v[10:11] op_sel_hi:[1,0,1]
	v_cvt_pk_bf16_f32 v10, v36, v37
	v_cvt_pk_bf16_f32 v11, v38, v39
	v_and_b32_e32 v35, 0xffff0000, v10
	v_lshlrev_b32_e32 v34, 16, v10
	v_mul_f32_e32 v35, v35, v35
	v_and_b32_e32 v52, 0xffff0000, v11
	v_fmac_f32_e32 v35, v34, v34
	v_lshlrev_b32_e32 v34, 16, v11
	v_mul_f32_e32 v52, v52, v52
	v_cvt_pk_bf16_f32 v12, v50, v51
	v_fmac_f32_e32 v52, v34, v34
	v_add_f32_e32 v34, v35, v52
	v_and_b32_e32 v52, 0xffff0000, v12
	v_cvt_pk_bf16_f32 v13, v32, v33
	v_lshlrev_b32_e32 v35, 16, v12
	v_mul_f32_e32 v52, v52, v52
	v_fmac_f32_e32 v52, v35, v35
	v_and_b32_e32 v35, 0xffff0000, v13
	v_add_f32_e32 v52, v34, v52
	v_lshlrev_b32_e32 v34, 16, v13
	v_mul_f32_e32 v53, v35, v35
	v_fmac_f32_e32 v53, v34, v34
	v_mul_f32_e32 v34, 4.0, v36
	v_mul_f32_e32 v35, 4.0, v37
	v_med3_f32 v37, v34, s34, v49
	v_med3_f32 v35, v35, s34, v49
	v_mov_b32_e32 v34, 0
	v_cvt_pk_fp8_f32 v34, v37, v35
	v_mul_f32_e32 v36, 4.0, v38
	v_mul_f32_e32 v35, 4.0, v39
	v_med3_f32 v36, v36, s34, v49
	v_med3_f32 v35, v35, s34, v49
	v_cvt_pk_fp8_f32 v34, v36, v35 op_sel:[0,0,1]
	v_mul_f32_e32 v35, 4.0, v50
	v_mul_f32_e32 v36, 4.0, v51
	v_med3_f32 v37, v35, s34, v49
	v_med3_f32 v36, v36, s34, v49
	v_mov_b32_e32 v35, 0
	v_cvt_pk_fp8_f32 v35, v37, v36
	v_mul_f32_e32 v32, 4.0, v32
	v_mul_f32_e32 v33, 4.0, v33
	v_med3_f32 v32, v32, s34, v49
	v_med3_f32 v33, v33, s34, v49
	v_cvt_pk_fp8_f32 v35, v32, v33 op_sel:[0,0,1]
	v_add_f32_e32 v32, v52, v53
	global_store_dwordx4 v[14:15], v[10:13], off offset:1024 nt
	global_store_dwordx2 v[16:17], v[34:35], off offset:512
	s_nop 0
	v_cvt_pk_f32_fp8_sdwa v[12:13], v28 src0_sel:WORD_1
	s_waitcnt vmcnt(5)
	v_cvt_pk_f32_fp8_sdwa v[36:37], v30 src0_sel:WORD_1
	v_add_f32_e32 v52, v60, v32
	v_cvt_pk_f32_fp8_e32 v[10:11], v28
	v_cvt_pk_f32_fp8_e32 v[32:33], v29
	v_cvt_pk_f32_fp8_e32 v[34:35], v30
	v_cvt_pk_f32_fp8_e32 v[38:39], v31
	v_cvt_pk_f32_fp8_sdwa v[28:29], v29 src0_sel:WORD_1
	v_cvt_pk_f32_fp8_sdwa v[30:31], v31 src0_sel:WORD_1
	v_lshlrev_b32_e32 v50, 16, v6
	v_and_b32_e32 v51, 0xffff0000, v6
	v_lshlrev_b32_e32 v6, 16, v7
	v_and_b32_e32 v7, 0xffff0000, v7
	v_pk_add_f32 v[12:13], v[12:13], v[36:37]
	v_pk_add_f32 v[10:11], v[10:11], v[34:35]
	v_pk_fma_f32 v[12:13], v[12:13], s[18:19], v[6:7] op_sel_hi:[1,0,1]
	v_lshlrev_b32_e32 v6, 16, v8
	v_and_b32_e32 v7, 0xffff0000, v8
	v_pk_add_f32 v[32:33], v[32:33], v[38:39]
	v_pk_fma_f32 v[10:11], v[10:11], s[18:19], v[50:51] op_sel_hi:[1,0,1]
	v_pk_fma_f32 v[32:33], v[32:33], s[18:19], v[6:7] op_sel_hi:[1,0,1]
	v_lshlrev_b32_e32 v6, 16, v9
	v_and_b32_e32 v7, 0xffff0000, v9
	v_pk_add_f32 v[8:9], v[28:29], v[30:31]
	s_waitcnt vmcnt(4)
	v_cvt_pk_f32_fp8_e32 v[36:37], v27
	v_pk_fma_f32 v[28:29], v[8:9], s[18:19], v[6:7] op_sel_hi:[1,0,1]
	v_cvt_pk_bf16_f32 v6, v10, v11
	v_cvt_pk_bf16_f32 v7, v12, v13
	v_and_b32_e32 v31, 0xffff0000, v6
	v_lshlrev_b32_e32 v30, 16, v6
	v_mul_f32_e32 v31, v31, v31
	v_and_b32_e32 v34, 0xffff0000, v7
	v_fmac_f32_e32 v31, v30, v30
	v_lshlrev_b32_e32 v30, 16, v7
	v_mul_f32_e32 v34, v34, v34
	v_cvt_pk_bf16_f32 v8, v32, v33
	v_fmac_f32_e32 v34, v30, v30
	v_add_f32_e32 v30, v31, v34
	v_and_b32_e32 v34, 0xffff0000, v8
	v_lshlrev_b32_e32 v31, 16, v8
	v_mul_f32_e32 v34, v34, v34
	v_cvt_pk_bf16_f32 v9, v28, v29
	v_fmac_f32_e32 v34, v31, v31
	v_add_f32_e32 v30, v30, v34
	v_and_b32_e32 v34, 0xffff0000, v9
	v_lshlrev_b32_e32 v31, 16, v9
	v_mul_f32_e32 v34, v34, v34
	v_fmac_f32_e32 v34, v31, v31
	v_add_f32_e32 v30, v30, v34
	v_mul_f32_e32 v10, 4.0, v10
	v_mul_f32_e32 v11, 4.0, v11
	v_add_f32_e32 v50, v52, v30
	v_med3_f32 v10, v10, s34, v49
	v_med3_f32 v11, v11, s34, v49
	v_mov_b32_e32 v30, 0
	v_cvt_pk_fp8_f32 v30, v10, v11
	v_mul_f32_e32 v12, 4.0, v12
	v_mul_f32_e32 v10, 4.0, v13
	v_med3_f32 v11, v12, s34, v49
	v_med3_f32 v10, v10, s34, v49
	v_cvt_pk_fp8_f32 v30, v11, v10 op_sel:[0,0,1]
	v_mul_f32_e32 v10, 4.0, v32
	v_mul_f32_e32 v11, 4.0, v33
	v_med3_f32 v10, v10, s34, v49
	v_med3_f32 v11, v11, s34, v49
	v_mov_b32_e32 v31, 0
	v_cvt_pk_fp8_f32 v31, v10, v11
	v_mul_f32_e32 v12, 4.0, v28
	v_mul_f32_e32 v10, 4.0, v29
	v_med3_f32 v11, v12, s34, v49
	v_med3_f32 v10, v10, s34, v49
	v_cvt_pk_fp8_f32 v31, v11, v10 op_sel:[0,0,1]
	v_cvt_pk_f32_fp8_e32 v[10:11], v24
	v_cvt_pk_f32_fp8_e32 v[32:33], v26
	v_cvt_pk_f32_fp8_sdwa v[12:13], v24 src0_sel:WORD_1
	v_cvt_pk_f32_fp8_sdwa v[34:35], v26 src0_sel:WORD_1
	v_cvt_pk_f32_fp8_e32 v[28:29], v25
	v_cvt_pk_f32_fp8_sdwa v[24:25], v25 src0_sel:WORD_1
	v_cvt_pk_f32_fp8_sdwa v[26:27], v27 src0_sel:WORD_1
	v_lshlrev_b32_e32 v38, 16, v2
	v_and_b32_e32 v39, 0xffff0000, v2
	v_pk_add_f32 v[10:11], v[10:11], v[32:33]
	v_lshlrev_b32_e32 v2, 16, v3
	v_pk_fma_f32 v[32:33], v[10:11], s[18:19], v[38:39] op_sel_hi:[1,0,1]
	v_and_b32_e32 v3, 0xffff0000, v3
	v_pk_add_f32 v[10:11], v[12:13], v[34:35]
	v_pk_add_f32 v[12:13], v[28:29], v[36:37]
	v_pk_fma_f32 v[2:3], v[10:11], s[18:19], v[2:3] op_sel_hi:[1,0,1]
	v_lshlrev_b32_e32 v10, 16, v4
	v_and_b32_e32 v11, 0xffff0000, v4
	v_pk_fma_f32 v[28:29], v[12:13], s[18:19], v[10:11] op_sel_hi:[1,0,1]
	v_lshlrev_b32_e32 v4, 16, v5
	v_and_b32_e32 v5, 0xffff0000, v5
	v_pk_add_f32 v[10:11], v[24:25], v[26:27]
	v_cvt_pk_bf16_f32 v12, v28, v29
	v_pk_fma_f32 v[4:5], v[10:11], s[18:19], v[4:5] op_sel_hi:[1,0,1]
	v_cvt_pk_bf16_f32 v10, v32, v33
	v_cvt_pk_bf16_f32 v11, v2, v3
	v_and_b32_e32 v25, 0xffff0000, v10
	v_lshlrev_b32_e32 v24, 16, v10
	v_mul_f32_e32 v25, v25, v25
	v_and_b32_e32 v26, 0xffff0000, v11
	v_fmac_f32_e32 v25, v24, v24
	v_lshlrev_b32_e32 v24, 16, v11
	v_mul_f32_e32 v26, v26, v26
	v_fmac_f32_e32 v26, v24, v24
	v_add_f32_e32 v24, v25, v26
	v_and_b32_e32 v26, 0xffff0000, v12
	v_lshlrev_b32_e32 v25, 16, v12
	v_mul_f32_e32 v26, v26, v26
	v_cvt_pk_bf16_f32 v13, v4, v5
	v_fmac_f32_e32 v26, v25, v25
	v_add_f32_e32 v24, v24, v26
	v_and_b32_e32 v26, 0xffff0000, v13
	v_lshlrev_b32_e32 v25, 16, v13
	v_mul_f32_e32 v26, v26, v26
	v_fmac_f32_e32 v26, v25, v25
	v_add_f32_e32 v24, v24, v26
	v_add_f32_e32 v24, v50, v24
	ds_bpermute_b32 v27, v43, v24
	v_mul_f32_e32 v25, 4.0, v32
	v_mul_f32_e32 v26, 4.0, v33
	v_med3_f32 v25, v25, s34, v49
	v_med3_f32 v26, v26, s34, v49
	s_waitcnt lgkmcnt(0)
	v_add_f32_e32 v27, v24, v27
	ds_bpermute_b32 v32, v44, v27
	v_mov_b32_e32 v24, 0
	v_cvt_pk_fp8_f32 v24, v25, v26
	v_mul_f32_e32 v2, 4.0, v2
	v_mul_f32_e32 v3, 4.0, v3
	s_waitcnt lgkmcnt(0)
	v_add_f32_e32 v25, v27, v32
	ds_bpermute_b32 v26, v45, v25
	v_med3_f32 v2, v2, s34, v49
	v_med3_f32 v3, v3, s34, v49
	v_cvt_pk_fp8_f32 v24, v2, v3 op_sel:[0,0,1]
	v_mul_f32_e32 v2, 4.0, v28
	s_waitcnt lgkmcnt(0)
	v_add_f32_e32 v26, v25, v26
	ds_bpermute_b32 v27, v46, v26
	v_mul_f32_e32 v3, 4.0, v29
	v_med3_f32 v2, v2, s34, v49
	v_med3_f32 v3, v3, s34, v49
	v_mov_b32_e32 v25, 0
	v_cvt_pk_fp8_f32 v25, v2, v3
	s_waitcnt lgkmcnt(0)
	v_add_f32_e32 v2, v26, v27
	ds_bpermute_b32 v3, v47, v2
	v_mul_f32_e32 v4, 4.0, v4
	v_mul_f32_e32 v5, 4.0, v5
	v_med3_f32 v4, v4, s34, v49
	v_med3_f32 v5, v5, s34, v49
	s_waitcnt lgkmcnt(0)
	v_add_f32_e32 v2, v2, v3
	ds_bpermute_b32 v3, v48, v2
	v_cvt_pk_fp8_f32 v25, v4, v5 op_sel:[0,0,1]
	global_store_dwordx4 v[14:15], v[6:9], off offset:2048 nt
	global_store_dwordx2 v[16:17], v[30:31], off offset:1024
	global_store_dwordx4 v[14:15], v[10:13], off offset:3072 nt
	global_store_dwordx2 v[16:17], v[24:25], off offset:1536
	s_and_saveexec_b64 s[30:31], s[4:5]
	s_cbranch_execz .LBB0_1080
	s_waitcnt lgkmcnt(0)
	v_add_f32_e32 v2, v2, v3
	v_fmamk_f32 v2, v2, 0x3a000000, v41
	v_mul_f32_e32 v3, 0x4f800000, v2
	v_cmp_gt_f32_e32 vcc, s36, v2
	s_nop 1
	v_cndmask_b32_e32 v2, v2, v3, vcc
	v_sqrt_f32_e32 v3, v2
	s_nop 0
	v_add_u32_e32 v4, -1, v3
	v_fma_f32 v6, -v4, v3, v2
	v_add_u32_e32 v5, 1, v3
	v_cmp_ge_f32_e64 s[6:7], 0, v6
	s_nop 1
	v_cndmask_b32_e64 v4, v3, v4, s[6:7]
	v_fma_f32 v3, -v5, v3, v2
	v_cmp_lt_f32_e64 s[6:7], 0, v3
	s_nop 1
	v_cndmask_b32_e64 v3, v4, v5, s[6:7]
	v_mul_f32_e32 v4, 0x37800000, v3
	v_cndmask_b32_e32 v3, v3, v4, vcc
	v_cmp_class_f32_e32 vcc, v2, v42
	s_nop 1
	v_cndmask_b32_e32 v2, v3, v2, vcc
	v_div_scale_f32 v3, s[6:7], v2, v2, 1.0
	v_rcp_f32_e32 v4, v3
	s_add_u32 s6, s82, s38
	s_addc_u32 s7, s83, s39
	v_fma_f32 v5, -v3, v4, 1.0
	v_fmac_f32_e32 v4, v5, v4
	v_div_scale_f32 v5, vcc, 1.0, v2, 1.0
	v_mul_f32_e32 v6, v5, v4
	v_fma_f32 v7, -v3, v6, v5
	v_fmac_f32_e32 v6, v7, v4
	v_fma_f32 v3, -v3, v6, v5
	v_div_fmas_f32 v3, v3, v4, v6
	v_div_fixup_f32 v2, v3, v2, 1.0
	global_store_dword v1, v2, s[6:7]
	s_branch .LBB0_1080

.LBB0_1689:
	s_or_b64 exec, exec, s[0:1]
	s_lshl_b32 s0, s87, 3
	s_add_i32 s0, s0, s88
	s_cmpk_gt_i32 s0, 0x7fff
	s_waitcnt lgkmcnt(0)
	s_barrier
	s_cbranch_scc1 .LBB0_1694
	s_add_u32 s2, s82, 0x57e00000
	s_addc_u32 s3, s83, 0
	s_add_u32 s15, s82, 0x2300000
	s_addc_u32 s18, s83, 0
	s_lshl_b32 s6, s0, 1
	s_ashr_i32 s7, s6, 31
	s_lshl_b32 s4, s84, 3
	s_lshl_b64 s[6:7], s[6:7], 2
	s_add_u32 s6, s15, s6
	v_mov_b32_e32 v17, 0
	s_addc_u32 s7, s18, s7
	global_load_dwordx2 v[0:1], v17, s[6:7] nt
	s_add_i32 s5, s0, s4
	s_ashr_i32 s1, s0, 31
	s_lshl_b32 s19, s84, 4
	s_lshl_b32 s8, s5, 1
	s_lshl_b64 s[10:11], s[0:1], 12
	s_add_u32 s10, s82, s10
	v_lshlrev_b32_e32 v16, 4, v246
	s_addc_u32 s11, s83, s11
	s_ashr_i32 s5, s4, 31
	s_lshl_b64 s[20:21], s[0:1], 13
	v_lshl_add_u64 v[2:3], s[10:11], 0, v[16:17]
	s_lshl_b64 s[10:11], s[4:5], 12
	s_add_u32 s20, s80, s20
	s_mov_b64 s[12:13], 0x46c00000
	v_lshlrev_b32_e32 v16, 5, v246
	s_addc_u32 s21, s81, s21
	s_mov_b64 s[16:17], 0x1000
	v_lshl_add_u64 v[18:19], v[2:3], 0, s[12:13]
	v_lshl_add_u64 v[2:3], s[20:21], 0, v[16:17]
	s_mov_b32 s7, 0
	v_lshlrev_b32_e32 v38, 3, v246
	s_lshl_b64 s[12:13], s[4:5], 13
	s_add_i32 s1, 0, 0x23c80
	v_lshl_add_u64 v[20:21], v[2:3], 0, s[16:17]
	s_mov_b32 s14, 0x3c800000
	s_waitcnt vmcnt(0)
	v_readfirstlane_b32 s5, v0
	v_readfirstlane_b32 s9, v1
	s_branch .LBB0_1692
.LBB0_1691:
	s_waitcnt vmcnt(7)
	v_cvt_pk_f32_fp8_e32 v[40:41], v34
	v_cvt_pk_f32_fp8_sdwa v[42:43], v34 src0_sel:WORD_1
	v_cvt_pk_f32_fp8_e32 v[44:45], v35
	v_cvt_pk_f32_fp8_sdwa v[46:47], v35 src0_sel:WORD_1
	s_waitcnt vmcnt(3)
	v_cvt_pk_f32_fp8_e32 v[34:35], v36
	v_cvt_pk_f32_fp8_sdwa v[48:49], v36 src0_sel:WORD_1
	v_cvt_pk_f32_fp8_e32 v[50:51], v37
	v_cvt_pk_f32_fp8_sdwa v[52:53], v37 src0_sel:WORD_1
	v_lshlrev_b32_e32 v36, 16, v12
	v_and_b32_e32 v37, 0xffff0000, v12
	v_pk_add_f32 v[34:35], v[40:41], v[34:35]
	v_lshlrev_b32_e32 v12, 16, v13
	v_pk_fma_f32 v[34:35], v[34:35], s[14:15], v[36:37] op_sel_hi:[1,0,1]
	v_and_b32_e32 v13, 0xffff0000, v13
	v_pk_add_f32 v[36:37], v[42:43], v[48:49]
	v_pk_add_f32 v[40:41], v[44:45], v[50:51]
	v_pk_fma_f32 v[36:37], v[36:37], s[14:15], v[12:13] op_sel_hi:[1,0,1]
	v_lshlrev_b32_e32 v12, 16, v14
	v_and_b32_e32 v13, 0xffff0000, v14
	v_pk_fma_f32 v[12:13], v[40:41], s[14:15], v[12:13] op_sel_hi:[1,0,1]
	v_lshlrev_b32_e32 v14, 16, v15
	v_and_b32_e32 v15, 0xffff0000, v15
	v_pk_add_f32 v[40:41], v[46:47], v[52:53]
	s_waitcnt vmcnt(2)
	v_cvt_pk_f32_fp8_e32 v[42:43], v33
	v_pk_fma_f32 v[14:15], v[40:41], s[14:15], v[14:15] op_sel_hi:[1,0,1]
	global_store_dwordx4 v[20:21], v[34:37], off offset:-4096 nt
	global_store_dwordx4 v[20:21], v[12:15], off offset:-4080 nt
	v_cvt_pk_f32_fp8_sdwa v[40:41], v32 src0_sel:WORD_1
	v_cvt_pk_f32_fp8_e32 v[34:35], v31
	v_cvt_pk_f32_fp8_sdwa v[14:15], v30 src0_sel:WORD_1
	v_cvt_pk_f32_fp8_e32 v[12:13], v30
	v_cvt_pk_f32_fp8_sdwa v[30:31], v31 src0_sel:WORD_1
	v_cvt_pk_f32_fp8_e32 v[36:37], v32
	v_cvt_pk_f32_fp8_sdwa v[32:33], v33 src0_sel:WORD_1
	v_lshlrev_b32_e32 v44, 16, v8
	v_and_b32_e32 v45, 0xffff0000, v8
	v_lshlrev_b32_e32 v8, 16, v9
	v_and_b32_e32 v9, 0xffff0000, v9
	v_pk_add_f32 v[14:15], v[14:15], v[40:41]
	v_pk_add_f32 v[12:13], v[12:13], v[36:37]
	v_pk_fma_f32 v[14:15], v[14:15], s[14:15], v[8:9] op_sel_hi:[1,0,1]
	v_lshlrev_b32_e32 v8, 16, v10
	v_and_b32_e32 v9, 0xffff0000, v10
	v_lshlrev_b32_e32 v10, 16, v11
	v_and_b32_e32 v11, 0xffff0000, v11
	v_pk_add_f32 v[30:31], v[30:31], v[32:33]
	v_pk_fma_f32 v[12:13], v[12:13], s[14:15], v[44:45] op_sel_hi:[1,0,1]
	v_pk_add_f32 v[34:35], v[34:35], v[42:43]
	v_pk_fma_f32 v[10:11], v[30:31], s[14:15], v[10:11] op_sel_hi:[1,0,1]
	v_pk_fma_f32 v[8:9], v[34:35], s[14:15], v[8:9] op_sel_hi:[1,0,1]
	global_store_dwordx4 v[20:21], v[12:15], off offset:-2048 nt
	global_store_dwordx4 v[20:21], v[8:11], off offset:-2032 nt
	s_waitcnt vmcnt(5)
	v_cvt_pk_f32_fp8_sdwa v[30:31], v28 src0_sel:WORD_1
	v_cvt_pk_f32_fp8_e32 v[12:13], v27
	v_cvt_pk_f32_fp8_sdwa v[10:11], v26 src0_sel:WORD_1
	v_cvt_pk_f32_fp8_e32 v[32:33], v29
	v_cvt_pk_f32_fp8_e32 v[8:9], v26
	v_cvt_pk_f32_fp8_sdwa v[14:15], v27 src0_sel:WORD_1
	v_cvt_pk_f32_fp8_e32 v[26:27], v28
	v_cvt_pk_f32_fp8_sdwa v[28:29], v29 src0_sel:WORD_1
	v_lshlrev_b32_e32 v34, 16, v4
	v_and_b32_e32 v35, 0xffff0000, v4
	v_lshlrev_b32_e32 v4, 16, v5
	v_and_b32_e32 v5, 0xffff0000, v5
	v_pk_add_f32 v[10:11], v[10:11], v[30:31]
	v_pk_add_f32 v[12:13], v[12:13], v[32:33]
	v_pk_fma_f32 v[10:11], v[10:11], s[14:15], v[4:5] op_sel_hi:[1,0,1]
	v_lshlrev_b32_e32 v4, 16, v6
	v_and_b32_e32 v5, 0xffff0000, v6
	v_pk_add_f32 v[8:9], v[8:9], v[26:27]
	v_pk_fma_f32 v[4:5], v[12:13], s[14:15], v[4:5] op_sel_hi:[1,0,1]
	v_lshlrev_b32_e32 v6, 16, v7
	v_and_b32_e32 v7, 0xffff0000, v7
	v_pk_add_f32 v[12:13], v[14:15], v[28:29]
	v_pk_fma_f32 v[8:9], v[8:9], s[14:15], v[34:35] op_sel_hi:[1,0,1]
	v_pk_fma_f32 v[6:7], v[12:13], s[14:15], v[6:7] op_sel_hi:[1,0,1]
	global_store_dwordx4 v[20:21], v[8:11], off nt
	global_store_dwordx4 v[20:21], v[4:7], off offset:16 nt
	s_waitcnt vmcnt(6)
	v_cvt_pk_f32_fp8_sdwa v[14:15], v24 src0_sel:WORD_1
	v_cvt_pk_f32_fp8_e32 v[8:9], v23
	v_cvt_pk_f32_fp8_sdwa v[6:7], v22 src0_sel:WORD_1
	v_cvt_pk_f32_fp8_e32 v[4:5], v22
	v_cvt_pk_f32_fp8_sdwa v[10:11], v23 src0_sel:WORD_1
	v_cvt_pk_f32_fp8_e32 v[12:13], v24
	v_cvt_pk_f32_fp8_e32 v[22:23], v25
	v_cvt_pk_f32_fp8_sdwa v[24:25], v25 src0_sel:WORD_1
	v_lshlrev_b32_e32 v26, 16, v0
	v_and_b32_e32 v27, 0xffff0000, v0
	v_lshlrev_b32_e32 v0, 16, v1
	v_and_b32_e32 v1, 0xffff0000, v1
	v_pk_add_f32 v[6:7], v[6:7], v[14:15]
	v_pk_add_f32 v[4:5], v[4:5], v[12:13]
	v_pk_fma_f32 v[6:7], v[6:7], s[14:15], v[0:1] op_sel_hi:[1,0,1]
	v_lshlrev_b32_e32 v0, 16, v2
	v_and_b32_e32 v1, 0xffff0000, v2
	v_pk_add_f32 v[8:9], v[8:9], v[22:23]
	v_pk_fma_f32 v[4:5], v[4:5], s[14:15], v[26:27] op_sel_hi:[1,0,1]
	v_pk_fma_f32 v[0:1], v[8:9], s[14:15], v[0:1] op_sel_hi:[1,0,1]
	v_lshlrev_b32_e32 v2, 16, v3
	v_and_b32_e32 v3, 0xffff0000, v3
	v_pk_add_f32 v[8:9], v[10:11], v[24:25]
	s_add_i32 s8, s8, s19
	v_pk_fma_f32 v[2:3], v[8:9], s[14:15], v[2:3] op_sel_hi:[1,0,1]
	global_store_dwordx4 v[20:21], v[4:7], off offset:2048 nt
	global_store_dwordx4 v[20:21], v[0:3], off offset:2064 nt
	v_lshl_add_u64 v[18:19], v[18:19], 0, s[10:11]
	s_andn2_b64 vcc, exec, s[16:17]
	v_lshl_add_u64 v[20:21], v[20:21], 0, s[12:13]
	s_cbranch_vccz .LBB0_1694
.LBB0_1692:
	s_ashr_i32 s6, s5, 16
	s_lshl_b32 s6, s6, 2
	s_add_i32 s6, s1, s6
	v_mov_b32_e32 v0, s6
	s_ashr_i32 s6, s9, 16
	s_lshl_b32 s6, s6, 2
	s_add_i32 s6, s1, s6
	v_mov_b32_e32 v1, s6
	ds_read_b32 v0, v0
	ds_read_b32 v2, v1
	s_lshl_b32 s6, s5, 11
	s_and_b32 s6, s6, 0x7fff800
	s_add_i32 s0, s0, s4
	s_waitcnt lgkmcnt(1)
	v_ashrrev_i32_e32 v1, 31, v0
	v_lshlrev_b64 v[0:1], 19, v[0:1]
	s_waitcnt lgkmcnt(0)
	v_ashrrev_i32_e32 v3, 31, v2
	v_lshl_add_u64 v[0:1], s[2:3], 0, v[0:1]
	v_lshl_add_u64 v[0:1], v[0:1], 0, s[6:7]
	v_lshlrev_b64 v[2:3], 19, v[2:3]
	s_lshl_b32 s6, s9, 11
	s_and_b32 s6, s6, 0x7fff800
	v_lshl_add_u64 v[2:3], s[2:3], 0, v[2:3]
	v_lshl_add_u64 v[2:3], v[2:3], 0, s[6:7]
	v_readfirstlane_b32 s16, v0
	v_readfirstlane_b32 s17, v1
	v_readfirstlane_b32 s20, v2
	v_readfirstlane_b32 s21, v3
	global_load_dwordx4 v[12:15], v[18:19], off nt
	global_load_dwordx4 v[8:11], v[18:19], off offset:1024 nt
	global_load_dwordx4 v[4:7], v[18:19], off offset:2048 nt
	global_load_dwordx4 v[0:3], v[18:19], off offset:3072 nt
	global_load_dwordx2 v[34:35], v38, s[16:17] nt
	global_load_dwordx2 v[30:31], v38, s[16:17] offset:512 nt
	global_load_dwordx2 v[26:27], v38, s[16:17] offset:1024 nt
	global_load_dwordx2 v[22:23], v38, s[16:17] offset:1536 nt
	global_load_dwordx2 v[36:37], v38, s[20:21] nt
	global_load_dwordx2 v[32:33], v38, s[20:21] offset:512 nt
	global_load_dwordx2 v[28:29], v38, s[20:21] offset:1024 nt
	global_load_dwordx2 v[24:25], v38, s[20:21] offset:1536 nt
	s_cmpk_gt_i32 s0, 0x7fff
	s_cselect_b64 s[16:17], -1, 0
	s_and_b64 vcc, exec, s[16:17]
	s_cbranch_vccnz .LBB0_1691
	s_ashr_i32 s9, s8, 31
	s_lshl_b64 s[20:21], s[8:9], 2
	s_add_u32 s20, s15, s20
	s_addc_u32 s21, s18, s21
	global_load_dwordx2 v[40:41], v17, s[20:21] nt
	s_waitcnt vmcnt(0)
	v_readfirstlane_b32 s5, v40
	v_readfirstlane_b32 s9, v41
	s_branch .LBB0_1691
